# GEMM K-loops: s_setprio 1 moved before the pre-MFMA barrier, redundant lgkmcnt(0) after it dropped, mid-block setprio flips dropped, s_setprio 0 after the closing barrier
# baseline (speedup 1.0000x reference)
.LBB0_441:
	s_ashr_i32 s27, s26, 31
	s_lshl_b64 s[28:29], s[26:27], 17
	s_add_u32 s28, s39, s28
	v_add_u32_e32 v157, s79, v155
	v_add_u32_e32 v232, s80, v155
	s_addc_u32 s29, s54, s29
	ds_read_b128 v[158:161], v157
	ds_read_b128 v[162:165], v157 offset:1024
	ds_read_b128 v[168:171], v157 offset:2048
	ds_read_b128 v[172:175], v157 offset:3072
	ds_read_b128 v[176:179], v232
	ds_read_b128 v[180:183], v232 offset:1024
	ds_read_b128 v[184:187], v232 offset:2048
	ds_read_b128 v[188:191], v232 offset:3072
	s_and_b64 s[30:31], s[6:7], exec
	s_cselect_b32 s37, s29, s17
	s_cselect_b32 s36, s28, s16
	s_ashr_i32 s25, s24, 31
	s_lshl_b64 s[30:31], s[24:25], 17
	s_add_u32 s30, s55, s30
	s_addc_u32 s31, s70, s31
	s_and_b64 s[34:35], s[6:7], exec
	s_cselect_b32 s35, s31, s15
	s_cselect_b32 s34, s30, s14
	s_add_u32 s94, s16, 0x10080
	s_addc_u32 s95, s17, 0
	s_mov_b32 m0, s81
	v_lshl_add_u64 v[166:167], s[94:95], 0, v[130:131]
	ds_read_b128 v[192:195], v156
	ds_read_b128 v[196:199], v156 offset:1024
	ds_read_b128 v[200:203], v156 offset:2048
	ds_read_b128 v[204:207], v156 offset:3072
	ds_read_b128 v[208:211], v156 offset:4096
	ds_read_b128 v[212:215], v156 offset:5120
	ds_read_b128 v[216:219], v156 offset:6144
	ds_read_b128 v[220:223], v156 offset:7168
	global_load_lds_dwordx4 v[166:167], off
	v_lshl_add_u64 v[166:167], s[94:95], 0, v[134:135]
	s_mov_b32 m0, s82
	s_nop 0
	global_load_lds_dwordx4 v[166:167], off
	s_waitcnt vmcnt(8)
	s_waitcnt lgkmcnt(0)
	s_setprio 1
	s_barrier
	v_mfma_f32_16x16x32_bf16 v[126:129], v[158:161], v[192:195], v[126:129]
	v_mfma_f32_16x16x32_bf16 v[122:125], v[168:171], v[192:195], v[122:125]
	v_mfma_f32_16x16x32_bf16 v[114:117], v[158:161], v[200:203], v[114:117]
	v_mfma_f32_16x16x32_bf16 v[106:109], v[168:171], v[200:203], v[106:109]
	v_mfma_f32_16x16x32_bf16 v[102:105], v[158:161], v[208:211], v[102:105]
	v_mfma_f32_16x16x32_bf16 v[90:93], v[168:171], v[208:211], v[90:93]
	v_mfma_f32_16x16x32_bf16 v[86:89], v[158:161], v[216:219], v[86:89]
	v_mfma_f32_16x16x32_bf16 v[74:77], v[168:171], v[216:219], v[74:77]
	v_mfma_f32_16x16x32_bf16 v[126:129], v[162:165], v[196:199], v[126:129]
	v_mfma_f32_16x16x32_bf16 v[122:125], v[172:175], v[196:199], v[122:125]
	v_mfma_f32_16x16x32_bf16 v[114:117], v[162:165], v[204:207], v[114:117]
	v_mfma_f32_16x16x32_bf16 v[106:109], v[172:175], v[204:207], v[106:109]
	v_mfma_f32_16x16x32_bf16 v[102:105], v[162:165], v[212:215], v[102:105]
	v_mfma_f32_16x16x32_bf16 v[90:93], v[172:175], v[212:215], v[90:93]
	v_mfma_f32_16x16x32_bf16 v[86:89], v[162:165], v[220:223], v[86:89]
	v_mfma_f32_16x16x32_bf16 v[74:77], v[172:175], v[220:223], v[74:77]
	v_mfma_f32_16x16x32_bf16 v[118:121], v[176:179], v[192:195], v[118:121]
	v_mfma_f32_16x16x32_bf16 v[110:113], v[184:187], v[192:195], v[110:113]
	v_mfma_f32_16x16x32_bf16 v[98:101], v[176:179], v[200:203], v[98:101]
	v_mfma_f32_16x16x32_bf16 v[94:97], v[184:187], v[200:203], v[94:97]
	v_mfma_f32_16x16x32_bf16 v[82:85], v[176:179], v[208:211], v[82:85]
	v_mfma_f32_16x16x32_bf16 v[78:81], v[184:187], v[208:211], v[78:81]
	v_mfma_f32_16x16x32_bf16 v[70:73], v[176:179], v[216:219], v[70:73]
	v_mfma_f32_16x16x32_bf16 v[66:69], v[184:187], v[216:219], v[66:69]
	v_mfma_f32_16x16x32_bf16 v[118:121], v[180:183], v[196:199], v[118:121]
	v_mfma_f32_16x16x32_bf16 v[110:113], v[188:191], v[196:199], v[110:113]
	v_mfma_f32_16x16x32_bf16 v[98:101], v[180:183], v[204:207], v[98:101]
	v_mfma_f32_16x16x32_bf16 v[94:97], v[188:191], v[204:207], v[94:97]
	v_mfma_f32_16x16x32_bf16 v[82:85], v[180:183], v[212:215], v[82:85]
	v_mfma_f32_16x16x32_bf16 v[78:81], v[188:191], v[212:215], v[78:81]
	v_mfma_f32_16x16x32_bf16 v[70:73], v[180:183], v[220:223], v[70:73]
	v_mfma_f32_16x16x32_bf16 v[66:69], v[188:191], v[220:223], v[66:69]
	s_barrier
	s_setprio 0
	v_lshl_add_u64 v[166:167], s[14:15], 0, v[132:133]
	s_mov_b32 m0, s83
	v_lshl_add_u64 v[224:225], v[166:167], 0, s[20:21]
	ds_read_b128 v[192:195], v156 offset:16384
	ds_read_b128 v[196:199], v156 offset:17408
	ds_read_b128 v[200:203], v156 offset:18432
	ds_read_b128 v[204:207], v156 offset:19456
	ds_read_b128 v[208:211], v156 offset:20480
	ds_read_b128 v[212:215], v156 offset:21504
	ds_read_b128 v[216:219], v156 offset:22528
	ds_read_b128 v[220:223], v156 offset:23552
	global_load_lds_dwordx4 v[224:225], off
	v_lshl_add_u64 v[224:225], s[14:15], 0, v[136:137]
	s_add_u32 s94, s14, 0x10100
	v_lshl_add_u64 v[226:227], v[224:225], 0, s[20:21]
	s_mov_b32 m0, s84
	s_addc_u32 s95, s15, 0
	global_load_lds_dwordx4 v[226:227], off
	v_lshl_add_u64 v[226:227], s[94:95], 0, v[132:133]
	s_mov_b32 m0, s85
	s_nop 0
	global_load_lds_dwordx4 v[226:227], off
	v_lshl_add_u64 v[226:227], s[94:95], 0, v[136:137]
	s_mov_b32 m0, s86
	s_nop 0
	global_load_lds_dwordx4 v[226:227], off
	v_lshl_add_u64 v[226:227], s[16:17], 0, v[130:131]
	v_lshl_add_u64 v[228:229], v[226:227], 0, s[20:21]
	s_mov_b32 m0, s1
	s_nop 0
	global_load_lds_dwordx4 v[228:229], off
	v_lshl_add_u64 v[228:229], s[16:17], 0, v[134:135]
	v_lshl_add_u64 v[230:231], v[228:229], 0, s[20:21]
	s_mov_b32 m0, s9
	s_nop 0
	global_load_lds_dwordx4 v[230:231], off
	s_waitcnt vmcnt(8)
	s_waitcnt lgkmcnt(0)
	s_setprio 1
	s_barrier
	v_mfma_f32_16x16x32_bf16 v[62:65], v[158:161], v[192:195], v[62:65]
	v_mfma_f32_16x16x32_bf16 v[58:61], v[168:171], v[192:195], v[58:61]
	v_mfma_f32_16x16x32_bf16 v[54:57], v[158:161], v[200:203], v[54:57]
	v_mfma_f32_16x16x32_bf16 v[42:45], v[168:171], v[200:203], v[42:45]
	v_mfma_f32_16x16x32_bf16 v[38:41], v[158:161], v[208:211], v[38:41]
	v_mfma_f32_16x16x32_bf16 v[26:29], v[168:171], v[208:211], v[26:29]
	v_mfma_f32_16x16x32_bf16 v[22:25], v[158:161], v[216:219], v[22:25]
	v_mfma_f32_16x16x32_bf16 v[10:13], v[168:171], v[216:219], v[10:13]
	v_mfma_f32_16x16x32_bf16 v[62:65], v[162:165], v[196:199], v[62:65]
	v_mfma_f32_16x16x32_bf16 v[58:61], v[172:175], v[196:199], v[58:61]
	v_mfma_f32_16x16x32_bf16 v[54:57], v[162:165], v[204:207], v[54:57]
	v_mfma_f32_16x16x32_bf16 v[42:45], v[172:175], v[204:207], v[42:45]
	v_mfma_f32_16x16x32_bf16 v[38:41], v[162:165], v[212:215], v[38:41]
	v_mfma_f32_16x16x32_bf16 v[26:29], v[172:175], v[212:215], v[26:29]
	v_mfma_f32_16x16x32_bf16 v[22:25], v[162:165], v[220:223], v[22:25]
	v_mfma_f32_16x16x32_bf16 v[10:13], v[172:175], v[220:223], v[10:13]
	v_mfma_f32_16x16x32_bf16 v[50:53], v[176:179], v[192:195], v[50:53]
	v_mfma_f32_16x16x32_bf16 v[46:49], v[184:187], v[192:195], v[46:49]
	v_mfma_f32_16x16x32_bf16 v[34:37], v[176:179], v[200:203], v[34:37]
	v_mfma_f32_16x16x32_bf16 v[30:33], v[184:187], v[200:203], v[30:33]
	v_mfma_f32_16x16x32_bf16 v[18:21], v[176:179], v[208:211], v[18:21]
	v_mfma_f32_16x16x32_bf16 v[14:17], v[184:187], v[208:211], v[14:17]
	v_mfma_f32_16x16x32_bf16 v[6:9], v[176:179], v[216:219], v[6:9]
	v_mfma_f32_16x16x32_bf16 v[2:5], v[184:187], v[216:219], v[2:5]
	v_mfma_f32_16x16x32_bf16 v[50:53], v[180:183], v[196:199], v[50:53]
	v_mfma_f32_16x16x32_bf16 v[46:49], v[188:191], v[196:199], v[46:49]
	v_mfma_f32_16x16x32_bf16 v[34:37], v[180:183], v[204:207], v[34:37]
	v_mfma_f32_16x16x32_bf16 v[30:33], v[188:191], v[204:207], v[30:33]
	v_mfma_f32_16x16x32_bf16 v[18:21], v[180:183], v[212:215], v[18:21]
	v_mfma_f32_16x16x32_bf16 v[14:17], v[188:191], v[212:215], v[14:17]
	v_mfma_f32_16x16x32_bf16 v[6:9], v[180:183], v[220:223], v[6:9]
	v_mfma_f32_16x16x32_bf16 v[2:5], v[188:191], v[220:223], v[2:5]
	s_barrier
	s_setprio 0
	s_add_i32 s27, 0, 0x1c000
	v_add_u32_e32 v233, s87, v155
	v_add_u32_e32 v234, s27, v155
	ds_read_b128 v[158:161], v233
	ds_read_b128 v[162:165], v233 offset:1024
	ds_read_b128 v[168:171], v233 offset:2048
	ds_read_b128 v[172:175], v233 offset:3072
	ds_read_b128 v[176:179], v234
	ds_read_b128 v[180:183], v234 offset:1024
	ds_read_b128 v[184:187], v234 offset:2048
	ds_read_b128 v[188:191], v234 offset:3072
	s_add_u32 s94, s16, 0x10100
	s_addc_u32 s95, s17, 0
	s_mov_b32 m0, s72
	v_lshl_add_u64 v[230:231], s[94:95], 0, v[130:131]
	ds_read_b128 v[192:195], v156 offset:32768
	ds_read_b128 v[196:199], v156 offset:33792
	ds_read_b128 v[200:203], v156 offset:34816
	ds_read_b128 v[204:207], v156 offset:35840
	ds_read_b128 v[208:211], v156 offset:36864
	ds_read_b128 v[212:215], v156 offset:37888
	ds_read_b128 v[216:219], v156 offset:38912
	ds_read_b128 v[220:223], v156 offset:39936
	global_load_lds_dwordx4 v[230:231], off
	v_lshl_add_u64 v[230:231], s[94:95], 0, v[134:135]
	s_mov_b32 m0, s74
	s_nop 0
	global_load_lds_dwordx4 v[230:231], off
	s_waitcnt vmcnt(8)
	s_waitcnt lgkmcnt(0)
	s_setprio 1
	s_barrier
	v_mfma_f32_16x16x32_bf16 v[126:129], v[158:161], v[192:195], v[126:129]
	v_mfma_f32_16x16x32_bf16 v[122:125], v[168:171], v[192:195], v[122:125]
	v_mfma_f32_16x16x32_bf16 v[114:117], v[158:161], v[200:203], v[114:117]
	v_mfma_f32_16x16x32_bf16 v[106:109], v[168:171], v[200:203], v[106:109]
	v_mfma_f32_16x16x32_bf16 v[102:105], v[158:161], v[208:211], v[102:105]
	v_mfma_f32_16x16x32_bf16 v[90:93], v[168:171], v[208:211], v[90:93]
	v_mfma_f32_16x16x32_bf16 v[86:89], v[158:161], v[216:219], v[86:89]
	v_mfma_f32_16x16x32_bf16 v[74:77], v[168:171], v[216:219], v[74:77]
	v_mfma_f32_16x16x32_bf16 v[126:129], v[162:165], v[196:199], v[126:129]
	v_mfma_f32_16x16x32_bf16 v[122:125], v[172:175], v[196:199], v[122:125]
	v_mfma_f32_16x16x32_bf16 v[114:117], v[162:165], v[204:207], v[114:117]
	v_mfma_f32_16x16x32_bf16 v[106:109], v[172:175], v[204:207], v[106:109]
	v_mfma_f32_16x16x32_bf16 v[102:105], v[162:165], v[212:215], v[102:105]
	v_mfma_f32_16x16x32_bf16 v[90:93], v[172:175], v[212:215], v[90:93]
	v_mfma_f32_16x16x32_bf16 v[86:89], v[162:165], v[220:223], v[86:89]
	v_mfma_f32_16x16x32_bf16 v[74:77], v[172:175], v[220:223], v[74:77]
	v_mfma_f32_16x16x32_bf16 v[118:121], v[176:179], v[192:195], v[118:121]
	v_mfma_f32_16x16x32_bf16 v[110:113], v[184:187], v[192:195], v[110:113]
	v_mfma_f32_16x16x32_bf16 v[98:101], v[176:179], v[200:203], v[98:101]
	v_mfma_f32_16x16x32_bf16 v[94:97], v[184:187], v[200:203], v[94:97]
	v_mfma_f32_16x16x32_bf16 v[82:85], v[176:179], v[208:211], v[82:85]
	v_mfma_f32_16x16x32_bf16 v[78:81], v[184:187], v[208:211], v[78:81]
	v_mfma_f32_16x16x32_bf16 v[70:73], v[176:179], v[216:219], v[70:73]
	v_mfma_f32_16x16x32_bf16 v[66:69], v[184:187], v[216:219], v[66:69]
	v_mfma_f32_16x16x32_bf16 v[118:121], v[180:183], v[196:199], v[118:121]
	v_mfma_f32_16x16x32_bf16 v[110:113], v[188:191], v[196:199], v[110:113]
	v_mfma_f32_16x16x32_bf16 v[98:101], v[180:183], v[204:207], v[98:101]
	v_mfma_f32_16x16x32_bf16 v[94:97], v[188:191], v[204:207], v[94:97]
	v_mfma_f32_16x16x32_bf16 v[82:85], v[180:183], v[212:215], v[82:85]
	v_mfma_f32_16x16x32_bf16 v[78:81], v[188:191], v[212:215], v[78:81]
	v_mfma_f32_16x16x32_bf16 v[70:73], v[180:183], v[220:223], v[70:73]
	v_mfma_f32_16x16x32_bf16 v[66:69], v[188:191], v[220:223], v[66:69]
	s_barrier
	s_setprio 0
	s_add_i32 s90, s87, s71
	s_add_i32 s25, s90, 0x2000
	v_lshl_add_u64 v[166:167], v[166:167], 0, s[22:23]
	s_mov_b32 m0, s90
	s_add_u32 s94, s14, 0x10180
	ds_read_b128 v[192:195], v156 offset:49152
	ds_read_b128 v[196:199], v156 offset:50176
	ds_read_b128 v[200:203], v156 offset:51200
	ds_read_b128 v[204:207], v156 offset:52224
	ds_read_b128 v[208:211], v156 offset:53248
	ds_read_b128 v[212:215], v156 offset:54272
	ds_read_b128 v[216:219], v156 offset:55296
	ds_read_b128 v[220:223], v156 offset:56320
	global_load_lds_dwordx4 v[166:167], off
	v_lshl_add_u64 v[166:167], v[224:225], 0, s[22:23]
	s_mov_b32 m0, s25
	s_addc_u32 s95, s15, 0
	s_add_i32 s27, s27, s71
	global_load_lds_dwordx4 v[166:167], off
	v_lshl_add_u64 v[166:167], s[94:95], 0, v[132:133]
	s_mov_b32 m0, s27
	s_add_i32 s88, s27, 0x2000
	global_load_lds_dwordx4 v[166:167], off
	v_lshl_add_u64 v[166:167], s[94:95], 0, v[136:137]
	s_mov_b32 m0, s88
	s_nop 0
	global_load_lds_dwordx4 v[166:167], off
	v_lshl_add_u64 v[166:167], v[226:227], 0, s[22:23]
	s_mov_b32 m0, s77
	s_nop 0
	global_load_lds_dwordx4 v[166:167], off
	v_lshl_add_u64 v[166:167], v[228:229], 0, s[22:23]
	s_mov_b32 m0, s78
	s_nop 0
	global_load_lds_dwordx4 v[166:167], off
	s_waitcnt vmcnt(8)
	s_waitcnt lgkmcnt(0)
	s_setprio 1
	s_barrier
	v_mfma_f32_16x16x32_bf16 v[62:65], v[158:161], v[192:195], v[62:65]
	v_mfma_f32_16x16x32_bf16 v[58:61], v[168:171], v[192:195], v[58:61]
	v_mfma_f32_16x16x32_bf16 v[54:57], v[158:161], v[200:203], v[54:57]
	v_mfma_f32_16x16x32_bf16 v[42:45], v[168:171], v[200:203], v[42:45]
	v_mfma_f32_16x16x32_bf16 v[38:41], v[158:161], v[208:211], v[38:41]
	v_mfma_f32_16x16x32_bf16 v[26:29], v[168:171], v[208:211], v[26:29]
	v_mfma_f32_16x16x32_bf16 v[22:25], v[158:161], v[216:219], v[22:25]
	v_mfma_f32_16x16x32_bf16 v[10:13], v[168:171], v[216:219], v[10:13]
	v_mfma_f32_16x16x32_bf16 v[62:65], v[162:165], v[196:199], v[62:65]
	v_mfma_f32_16x16x32_bf16 v[58:61], v[172:175], v[196:199], v[58:61]
	v_mfma_f32_16x16x32_bf16 v[54:57], v[162:165], v[204:207], v[54:57]
	v_mfma_f32_16x16x32_bf16 v[42:45], v[172:175], v[204:207], v[42:45]
	v_mfma_f32_16x16x32_bf16 v[38:41], v[162:165], v[212:215], v[38:41]
	v_mfma_f32_16x16x32_bf16 v[26:29], v[172:175], v[212:215], v[26:29]
	v_mfma_f32_16x16x32_bf16 v[22:25], v[162:165], v[220:223], v[22:25]
	v_mfma_f32_16x16x32_bf16 v[10:13], v[172:175], v[220:223], v[10:13]
	v_mfma_f32_16x16x32_bf16 v[50:53], v[176:179], v[192:195], v[50:53]
	v_mfma_f32_16x16x32_bf16 v[46:49], v[184:187], v[192:195], v[46:49]
	v_mfma_f32_16x16x32_bf16 v[34:37], v[176:179], v[200:203], v[34:37]
	v_mfma_f32_16x16x32_bf16 v[30:33], v[184:187], v[200:203], v[30:33]
	v_mfma_f32_16x16x32_bf16 v[18:21], v[176:179], v[208:211], v[18:21]
	v_mfma_f32_16x16x32_bf16 v[14:17], v[184:187], v[208:211], v[14:17]
	v_mfma_f32_16x16x32_bf16 v[6:9], v[176:179], v[216:219], v[6:9]
	v_mfma_f32_16x16x32_bf16 v[2:5], v[184:187], v[216:219], v[2:5]
	v_mfma_f32_16x16x32_bf16 v[50:53], v[180:183], v[196:199], v[50:53]
	v_mfma_f32_16x16x32_bf16 v[46:49], v[188:191], v[196:199], v[46:49]
	v_mfma_f32_16x16x32_bf16 v[34:37], v[180:183], v[204:207], v[34:37]
	v_mfma_f32_16x16x32_bf16 v[30:33], v[188:191], v[204:207], v[30:33]
	v_mfma_f32_16x16x32_bf16 v[18:21], v[180:183], v[212:215], v[18:21]
	v_mfma_f32_16x16x32_bf16 v[14:17], v[188:191], v[212:215], v[14:17]
	v_mfma_f32_16x16x32_bf16 v[6:9], v[180:183], v[220:223], v[6:9]
	v_mfma_f32_16x16x32_bf16 v[2:5], v[188:191], v[220:223], v[2:5]
	s_barrier
	s_setprio 0
	ds_read_b128 v[158:161], v157
	ds_read_b128 v[162:165], v157 offset:1024
	ds_read_b128 v[168:171], v157 offset:2048
	ds_read_b128 v[172:175], v157 offset:3072
	ds_read_b128 v[176:179], v232
	ds_read_b128 v[180:183], v232 offset:1024
	ds_read_b128 v[184:187], v232 offset:2048
	ds_read_b128 v[188:191], v232 offset:3072
	s_add_u32 s94, s16, 0x10180
	s_addc_u32 s95, s17, 0
	s_mov_b32 m0, s81
	v_lshl_add_u64 v[166:167], s[94:95], 0, v[130:131]
	ds_read_b128 v[192:195], v156
	ds_read_b128 v[196:199], v156 offset:1024
	ds_read_b128 v[200:203], v156 offset:2048
	ds_read_b128 v[204:207], v156 offset:3072
	ds_read_b128 v[208:211], v156 offset:4096
	ds_read_b128 v[212:215], v156 offset:5120
	ds_read_b128 v[216:219], v156 offset:6144
	ds_read_b128 v[220:223], v156 offset:7168
	global_load_lds_dwordx4 v[166:167], off
	v_lshl_add_u64 v[166:167], s[94:95], 0, v[134:135]
	s_mov_b32 m0, s82
	s_nop 0
	global_load_lds_dwordx4 v[166:167], off
	s_waitcnt vmcnt(8)
	s_waitcnt lgkmcnt(0)
	s_setprio 1
	s_barrier
	v_mfma_f32_16x16x32_bf16 v[126:129], v[158:161], v[192:195], v[126:129]
	v_mfma_f32_16x16x32_bf16 v[122:125], v[168:171], v[192:195], v[122:125]
	v_mfma_f32_16x16x32_bf16 v[114:117], v[158:161], v[200:203], v[114:117]
	v_mfma_f32_16x16x32_bf16 v[106:109], v[168:171], v[200:203], v[106:109]
	v_mfma_f32_16x16x32_bf16 v[102:105], v[158:161], v[208:211], v[102:105]
	v_mfma_f32_16x16x32_bf16 v[90:93], v[168:171], v[208:211], v[90:93]
	v_mfma_f32_16x16x32_bf16 v[86:89], v[158:161], v[216:219], v[86:89]
	v_mfma_f32_16x16x32_bf16 v[74:77], v[168:171], v[216:219], v[74:77]
	v_mfma_f32_16x16x32_bf16 v[126:129], v[162:165], v[196:199], v[126:129]
	v_mfma_f32_16x16x32_bf16 v[122:125], v[172:175], v[196:199], v[122:125]
	v_mfma_f32_16x16x32_bf16 v[114:117], v[162:165], v[204:207], v[114:117]
	v_mfma_f32_16x16x32_bf16 v[106:109], v[172:175], v[204:207], v[106:109]
	v_mfma_f32_16x16x32_bf16 v[102:105], v[162:165], v[212:215], v[102:105]
	v_mfma_f32_16x16x32_bf16 v[90:93], v[172:175], v[212:215], v[90:93]
	v_mfma_f32_16x16x32_bf16 v[86:89], v[162:165], v[220:223], v[86:89]
	v_mfma_f32_16x16x32_bf16 v[74:77], v[172:175], v[220:223], v[74:77]
	v_mfma_f32_16x16x32_bf16 v[118:121], v[176:179], v[192:195], v[118:121]
	v_mfma_f32_16x16x32_bf16 v[110:113], v[184:187], v[192:195], v[110:113]
	v_mfma_f32_16x16x32_bf16 v[98:101], v[176:179], v[200:203], v[98:101]
	v_mfma_f32_16x16x32_bf16 v[94:97], v[184:187], v[200:203], v[94:97]
	v_mfma_f32_16x16x32_bf16 v[82:85], v[176:179], v[208:211], v[82:85]
	v_mfma_f32_16x16x32_bf16 v[78:81], v[184:187], v[208:211], v[78:81]
	v_mfma_f32_16x16x32_bf16 v[70:73], v[176:179], v[216:219], v[70:73]
	v_mfma_f32_16x16x32_bf16 v[66:69], v[184:187], v[216:219], v[66:69]
	v_mfma_f32_16x16x32_bf16 v[118:121], v[180:183], v[196:199], v[118:121]
	v_mfma_f32_16x16x32_bf16 v[110:113], v[188:191], v[196:199], v[110:113]
	v_mfma_f32_16x16x32_bf16 v[98:101], v[180:183], v[204:207], v[98:101]
	v_mfma_f32_16x16x32_bf16 v[94:97], v[188:191], v[204:207], v[94:97]
	v_mfma_f32_16x16x32_bf16 v[82:85], v[180:183], v[212:215], v[82:85]
	v_mfma_f32_16x16x32_bf16 v[78:81], v[188:191], v[212:215], v[78:81]
	v_mfma_f32_16x16x32_bf16 v[70:73], v[180:183], v[220:223], v[70:73]
	v_mfma_f32_16x16x32_bf16 v[66:69], v[188:191], v[220:223], v[66:69]
	s_barrier
	s_setprio 0
	s_mov_b32 m0, s83
	v_lshl_add_u64 v[166:167], s[34:35], 0, v[132:133]
	s_add_u32 s94, s34, 0x10000
	ds_read_b128 v[192:195], v156 offset:16384
	ds_read_b128 v[196:199], v156 offset:17408
	ds_read_b128 v[200:203], v156 offset:18432
	ds_read_b128 v[204:207], v156 offset:19456
	ds_read_b128 v[208:211], v156 offset:20480
	ds_read_b128 v[212:215], v156 offset:21504
	ds_read_b128 v[216:219], v156 offset:22528
	ds_read_b128 v[220:223], v156 offset:23552
	global_load_lds_dwordx4 v[166:167], off
	v_lshl_add_u64 v[224:225], s[34:35], 0, v[136:137]
	s_mov_b32 m0, s84
	s_addc_u32 s95, s35, 0
	global_load_lds_dwordx4 v[224:225], off
	v_lshl_add_u64 v[226:227], s[94:95], 0, v[132:133]
	s_mov_b32 m0, s85
	v_lshl_add_u64 v[228:229], s[36:37], 0, v[134:135]
	global_load_lds_dwordx4 v[226:227], off
	v_lshl_add_u64 v[226:227], s[94:95], 0, v[136:137]
	s_mov_b32 m0, s86
	s_nop 0
	global_load_lds_dwordx4 v[226:227], off
	v_lshl_add_u64 v[226:227], s[36:37], 0, v[130:131]
	s_mov_b32 m0, s1
	s_nop 0
	global_load_lds_dwordx4 v[226:227], off
	s_mov_b32 m0, s9
	s_nop 0
	global_load_lds_dwordx4 v[228:229], off
	s_waitcnt vmcnt(8)
	s_waitcnt lgkmcnt(0)
	s_setprio 1
	s_barrier
	v_mfma_f32_16x16x32_bf16 v[62:65], v[158:161], v[192:195], v[62:65]
	v_mfma_f32_16x16x32_bf16 v[58:61], v[168:171], v[192:195], v[58:61]
	v_mfma_f32_16x16x32_bf16 v[54:57], v[158:161], v[200:203], v[54:57]
	v_mfma_f32_16x16x32_bf16 v[42:45], v[168:171], v[200:203], v[42:45]
	v_mfma_f32_16x16x32_bf16 v[38:41], v[158:161], v[208:211], v[38:41]
	v_mfma_f32_16x16x32_bf16 v[26:29], v[168:171], v[208:211], v[26:29]
	v_mfma_f32_16x16x32_bf16 v[22:25], v[158:161], v[216:219], v[22:25]
	v_mfma_f32_16x16x32_bf16 v[10:13], v[168:171], v[216:219], v[10:13]
	v_mfma_f32_16x16x32_bf16 v[62:65], v[162:165], v[196:199], v[62:65]
	v_mfma_f32_16x16x32_bf16 v[58:61], v[172:175], v[196:199], v[58:61]
	v_mfma_f32_16x16x32_bf16 v[54:57], v[162:165], v[204:207], v[54:57]
	v_mfma_f32_16x16x32_bf16 v[42:45], v[172:175], v[204:207], v[42:45]
	v_mfma_f32_16x16x32_bf16 v[38:41], v[162:165], v[212:215], v[38:41]
	v_mfma_f32_16x16x32_bf16 v[26:29], v[172:175], v[212:215], v[26:29]
	v_mfma_f32_16x16x32_bf16 v[22:25], v[162:165], v[220:223], v[22:25]
	v_mfma_f32_16x16x32_bf16 v[10:13], v[172:175], v[220:223], v[10:13]
	v_mfma_f32_16x16x32_bf16 v[50:53], v[176:179], v[192:195], v[50:53]
	v_mfma_f32_16x16x32_bf16 v[46:49], v[184:187], v[192:195], v[46:49]
	v_mfma_f32_16x16x32_bf16 v[34:37], v[176:179], v[200:203], v[34:37]
	v_mfma_f32_16x16x32_bf16 v[30:33], v[184:187], v[200:203], v[30:33]
	v_mfma_f32_16x16x32_bf16 v[18:21], v[176:179], v[208:211], v[18:21]
	v_mfma_f32_16x16x32_bf16 v[14:17], v[184:187], v[208:211], v[14:17]
	v_mfma_f32_16x16x32_bf16 v[6:9], v[176:179], v[216:219], v[6:9]
	v_mfma_f32_16x16x32_bf16 v[2:5], v[184:187], v[216:219], v[2:5]
	v_mfma_f32_16x16x32_bf16 v[50:53], v[180:183], v[196:199], v[50:53]
	v_mfma_f32_16x16x32_bf16 v[46:49], v[188:191], v[196:199], v[46:49]
	v_mfma_f32_16x16x32_bf16 v[34:37], v[180:183], v[204:207], v[34:37]
	v_mfma_f32_16x16x32_bf16 v[30:33], v[188:191], v[204:207], v[30:33]
	v_mfma_f32_16x16x32_bf16 v[18:21], v[180:183], v[212:215], v[18:21]
	v_mfma_f32_16x16x32_bf16 v[14:17], v[188:191], v[212:215], v[14:17]
	v_mfma_f32_16x16x32_bf16 v[6:9], v[180:183], v[220:223], v[6:9]
	v_mfma_f32_16x16x32_bf16 v[2:5], v[188:191], v[220:223], v[2:5]
	s_barrier
	s_setprio 0
	ds_read_b128 v[158:161], v233
	ds_read_b128 v[162:165], v233 offset:1024
	ds_read_b128 v[168:171], v233 offset:2048
	ds_read_b128 v[172:175], v233 offset:3072
	ds_read_b128 v[176:179], v234
	ds_read_b128 v[180:183], v234 offset:1024
	ds_read_b128 v[184:187], v234 offset:2048
	ds_read_b128 v[188:191], v234 offset:3072
	s_add_u32 s36, s36, 0x10000
	s_addc_u32 s37, s37, 0
	s_mov_b32 m0, s72
	v_lshl_add_u64 v[230:231], s[36:37], 0, v[130:131]
	ds_read_b128 v[192:195], v156 offset:32768
	ds_read_b128 v[196:199], v156 offset:33792
	ds_read_b128 v[200:203], v156 offset:34816
	ds_read_b128 v[204:207], v156 offset:35840
	ds_read_b128 v[208:211], v156 offset:36864
	ds_read_b128 v[212:215], v156 offset:37888
	ds_read_b128 v[216:219], v156 offset:38912
	ds_read_b128 v[220:223], v156 offset:39936
	global_load_lds_dwordx4 v[230:231], off
	v_lshl_add_u64 v[230:231], s[36:37], 0, v[134:135]
	s_mov_b32 m0, s74
	s_nop 0
	global_load_lds_dwordx4 v[230:231], off
	s_waitcnt vmcnt(8)
	s_waitcnt lgkmcnt(0)
	s_setprio 1
	s_barrier
	v_mfma_f32_16x16x32_bf16 v[126:129], v[158:161], v[192:195], v[126:129]
	v_mfma_f32_16x16x32_bf16 v[122:125], v[168:171], v[192:195], v[122:125]
	v_mfma_f32_16x16x32_bf16 v[114:117], v[158:161], v[200:203], v[114:117]
	v_mfma_f32_16x16x32_bf16 v[106:109], v[168:171], v[200:203], v[106:109]
	v_mfma_f32_16x16x32_bf16 v[102:105], v[158:161], v[208:211], v[102:105]
	v_mfma_f32_16x16x32_bf16 v[90:93], v[168:171], v[208:211], v[90:93]
	v_mfma_f32_16x16x32_bf16 v[86:89], v[158:161], v[216:219], v[86:89]
	v_mfma_f32_16x16x32_bf16 v[74:77], v[168:171], v[216:219], v[74:77]
	v_mfma_f32_16x16x32_bf16 v[126:129], v[162:165], v[196:199], v[126:129]
	v_mfma_f32_16x16x32_bf16 v[122:125], v[172:175], v[196:199], v[122:125]
	v_mfma_f32_16x16x32_bf16 v[114:117], v[162:165], v[204:207], v[114:117]
	v_mfma_f32_16x16x32_bf16 v[106:109], v[172:175], v[204:207], v[106:109]
	v_mfma_f32_16x16x32_bf16 v[102:105], v[162:165], v[212:215], v[102:105]
	v_mfma_f32_16x16x32_bf16 v[90:93], v[172:175], v[212:215], v[90:93]
	v_mfma_f32_16x16x32_bf16 v[86:89], v[162:165], v[220:223], v[86:89]
	v_mfma_f32_16x16x32_bf16 v[74:77], v[172:175], v[220:223], v[74:77]
	v_mfma_f32_16x16x32_bf16 v[118:121], v[176:179], v[192:195], v[118:121]
	v_mfma_f32_16x16x32_bf16 v[110:113], v[184:187], v[192:195], v[110:113]
	v_mfma_f32_16x16x32_bf16 v[98:101], v[176:179], v[200:203], v[98:101]
	v_mfma_f32_16x16x32_bf16 v[94:97], v[184:187], v[200:203], v[94:97]
	v_mfma_f32_16x16x32_bf16 v[82:85], v[176:179], v[208:211], v[82:85]
	v_mfma_f32_16x16x32_bf16 v[78:81], v[184:187], v[208:211], v[78:81]
	v_mfma_f32_16x16x32_bf16 v[70:73], v[176:179], v[216:219], v[70:73]
	v_mfma_f32_16x16x32_bf16 v[66:69], v[184:187], v[216:219], v[66:69]
	v_mfma_f32_16x16x32_bf16 v[118:121], v[180:183], v[196:199], v[118:121]
	v_mfma_f32_16x16x32_bf16 v[110:113], v[188:191], v[196:199], v[110:113]
	v_mfma_f32_16x16x32_bf16 v[98:101], v[180:183], v[204:207], v[98:101]
	v_mfma_f32_16x16x32_bf16 v[94:97], v[188:191], v[204:207], v[94:97]
	v_mfma_f32_16x16x32_bf16 v[82:85], v[180:183], v[212:215], v[82:85]
	v_mfma_f32_16x16x32_bf16 v[78:81], v[188:191], v[212:215], v[78:81]
	v_mfma_f32_16x16x32_bf16 v[70:73], v[180:183], v[220:223], v[70:73]
	v_mfma_f32_16x16x32_bf16 v[66:69], v[188:191], v[220:223], v[66:69]
	s_barrier
	s_setprio 0
	s_mov_b32 m0, s90
	v_lshl_add_u64 v[166:167], v[166:167], 0, s[18:19]
	s_add_u32 s34, s34, 0x10080
	ds_read_b128 v[192:195], v156 offset:49152
	ds_read_b128 v[196:199], v156 offset:50176
	ds_read_b128 v[200:203], v156 offset:51200
	ds_read_b128 v[204:207], v156 offset:52224
	ds_read_b128 v[208:211], v156 offset:53248
	ds_read_b128 v[212:215], v156 offset:54272
	ds_read_b128 v[216:219], v156 offset:55296
	ds_read_b128 v[220:223], v156 offset:56320
	global_load_lds_dwordx4 v[166:167], off
	v_lshl_add_u64 v[166:167], v[224:225], 0, s[18:19]
	s_mov_b32 m0, s25
	s_addc_u32 s35, s35, 0
	global_load_lds_dwordx4 v[166:167], off
	v_lshl_add_u64 v[166:167], s[34:35], 0, v[132:133]
	s_mov_b32 m0, s27
	s_nop 0
	global_load_lds_dwordx4 v[166:167], off
	v_lshl_add_u64 v[166:167], s[34:35], 0, v[136:137]
	s_mov_b32 m0, s88
	s_nop 0
	global_load_lds_dwordx4 v[166:167], off
	v_lshl_add_u64 v[166:167], v[226:227], 0, s[18:19]
	s_mov_b32 m0, s77
	s_nop 0
	global_load_lds_dwordx4 v[166:167], off
	v_lshl_add_u64 v[166:167], v[228:229], 0, s[18:19]
	s_mov_b32 m0, s78
	s_nop 0
	global_load_lds_dwordx4 v[166:167], off
	s_waitcnt vmcnt(8)
	s_waitcnt lgkmcnt(0)
	s_setprio 1
	s_barrier
	v_mfma_f32_16x16x32_bf16 v[62:65], v[158:161], v[192:195], v[62:65]
	v_mfma_f32_16x16x32_bf16 v[58:61], v[168:171], v[192:195], v[58:61]
	v_mfma_f32_16x16x32_bf16 v[54:57], v[158:161], v[200:203], v[54:57]
	v_mfma_f32_16x16x32_bf16 v[42:45], v[168:171], v[200:203], v[42:45]
	v_mfma_f32_16x16x32_bf16 v[38:41], v[158:161], v[208:211], v[38:41]
	v_mfma_f32_16x16x32_bf16 v[26:29], v[168:171], v[208:211], v[26:29]
	v_mfma_f32_16x16x32_bf16 v[22:25], v[158:161], v[216:219], v[22:25]
	v_mfma_f32_16x16x32_bf16 v[10:13], v[168:171], v[216:219], v[10:13]
	v_mfma_f32_16x16x32_bf16 v[62:65], v[162:165], v[196:199], v[62:65]
	v_mfma_f32_16x16x32_bf16 v[58:61], v[172:175], v[196:199], v[58:61]
	v_mfma_f32_16x16x32_bf16 v[54:57], v[162:165], v[204:207], v[54:57]
	v_mfma_f32_16x16x32_bf16 v[42:45], v[172:175], v[204:207], v[42:45]
	v_mfma_f32_16x16x32_bf16 v[38:41], v[162:165], v[212:215], v[38:41]
	v_mfma_f32_16x16x32_bf16 v[26:29], v[172:175], v[212:215], v[26:29]
	v_mfma_f32_16x16x32_bf16 v[22:25], v[162:165], v[220:223], v[22:25]
	v_mfma_f32_16x16x32_bf16 v[10:13], v[172:175], v[220:223], v[10:13]
	v_mfma_f32_16x16x32_bf16 v[50:53], v[176:179], v[192:195], v[50:53]
	v_mfma_f32_16x16x32_bf16 v[46:49], v[184:187], v[192:195], v[46:49]
	v_mfma_f32_16x16x32_bf16 v[34:37], v[176:179], v[200:203], v[34:37]
	v_mfma_f32_16x16x32_bf16 v[30:33], v[184:187], v[200:203], v[30:33]
	v_mfma_f32_16x16x32_bf16 v[18:21], v[176:179], v[208:211], v[18:21]
	v_mfma_f32_16x16x32_bf16 v[14:17], v[184:187], v[208:211], v[14:17]
	v_mfma_f32_16x16x32_bf16 v[6:9], v[176:179], v[216:219], v[6:9]
	v_mfma_f32_16x16x32_bf16 v[2:5], v[184:187], v[216:219], v[2:5]
	v_mfma_f32_16x16x32_bf16 v[50:53], v[180:183], v[196:199], v[50:53]
	v_mfma_f32_16x16x32_bf16 v[46:49], v[188:191], v[196:199], v[46:49]
	v_mfma_f32_16x16x32_bf16 v[34:37], v[180:183], v[204:207], v[34:37]
	v_mfma_f32_16x16x32_bf16 v[30:33], v[188:191], v[204:207], v[30:33]
	v_mfma_f32_16x16x32_bf16 v[18:21], v[180:183], v[212:215], v[18:21]
	v_mfma_f32_16x16x32_bf16 v[14:17], v[188:191], v[212:215], v[14:17]
	v_mfma_f32_16x16x32_bf16 v[6:9], v[180:183], v[220:223], v[6:9]
	v_mfma_f32_16x16x32_bf16 v[2:5], v[188:191], v[220:223], v[2:5]
	s_barrier
	s_setprio 0
	s_andn2_b64 vcc, exec, s[6:7]
	s_cbranch_vccnz .LBB0_434
	s_nop 3
	v_mov_b32_e32 v2, 0
	s_mov_b32 s8, s24
	s_mov_b32 s0, s26
	s_mov_b64 s[14:15], s[30:31]
	s_mov_b64 s[16:17], s[28:29]
	s_mov_b32 s76, s33
	v_mov_b32_e32 v3, v2
	v_mov_b32_e32 v4, v2
	v_mov_b32_e32 v5, v2
	v_mov_b32_e32 v6, v2
	v_mov_b32_e32 v7, v2
	v_mov_b32_e32 v8, v2
	v_mov_b32_e32 v9, v2
	v_mov_b32_e32 v14, v2
	v_mov_b32_e32 v15, v2
	v_mov_b32_e32 v16, v2
	v_mov_b32_e32 v17, v2
	v_mov_b32_e32 v18, v2
	v_mov_b32_e32 v19, v2
	v_mov_b32_e32 v20, v2
	v_mov_b32_e32 v21, v2
	v_mov_b32_e32 v30, v2
	v_mov_b32_e32 v31, v2
	v_mov_b32_e32 v32, v2
	v_mov_b32_e32 v33, v2
	v_mov_b32_e32 v34, v2
	v_mov_b32_e32 v35, v2
	v_mov_b32_e32 v36, v2
	v_mov_b32_e32 v37, v2
	v_mov_b32_e32 v46, v2
	v_mov_b32_e32 v47, v2
	v_mov_b32_e32 v48, v2
	v_mov_b32_e32 v49, v2
	v_mov_b32_e32 v50, v2
	v_mov_b32_e32 v51, v2
	v_mov_b32_e32 v52, v2
	v_mov_b32_e32 v53, v2
	v_mov_b32_e32 v10, v2
	v_mov_b32_e32 v11, v2
	v_mov_b32_e32 v12, v2
	v_mov_b32_e32 v13, v2
	v_mov_b32_e32 v22, v2
	v_mov_b32_e32 v23, v2
	v_mov_b32_e32 v24, v2
	v_mov_b32_e32 v25, v2
	v_mov_b32_e32 v26, v2
	v_mov_b32_e32 v27, v2
	v_mov_b32_e32 v28, v2
	v_mov_b32_e32 v29, v2
	v_mov_b32_e32 v38, v2
	v_mov_b32_e32 v39, v2
	v_mov_b32_e32 v40, v2
	v_mov_b32_e32 v41, v2
	v_mov_b32_e32 v42, v2
	v_mov_b32_e32 v43, v2
	v_mov_b32_e32 v44, v2
	v_mov_b32_e32 v45, v2
	v_mov_b32_e32 v54, v2
	v_mov_b32_e32 v55, v2
	v_mov_b32_e32 v56, v2
	v_mov_b32_e32 v57, v2
	v_mov_b32_e32 v58, v2
	v_mov_b32_e32 v59, v2
	v_mov_b32_e32 v60, v2
	v_mov_b32_e32 v61, v2
	v_mov_b32_e32 v62, v2
	v_mov_b32_e32 v63, v2
	v_mov_b32_e32 v64, v2
	v_mov_b32_e32 v65, v2
	v_mov_b32_e32 v66, v2
	v_mov_b32_e32 v67, v2
	v_mov_b32_e32 v68, v2
	v_mov_b32_e32 v69, v2
	v_mov_b32_e32 v70, v2
	v_mov_b32_e32 v71, v2
	v_mov_b32_e32 v72, v2
	v_mov_b32_e32 v73, v2
	v_mov_b32_e32 v78, v2
	v_mov_b32_e32 v79, v2
	v_mov_b32_e32 v80, v2
	v_mov_b32_e32 v81, v2
	v_mov_b32_e32 v82, v2
	v_mov_b32_e32 v83, v2
	v_mov_b32_e32 v84, v2
	v_mov_b32_e32 v85, v2
	v_mov_b32_e32 v94, v2
	v_mov_b32_e32 v95, v2
	v_mov_b32_e32 v96, v2
	v_mov_b32_e32 v97, v2
	v_mov_b32_e32 v98, v2
	v_mov_b32_e32 v99, v2
	v_mov_b32_e32 v100, v2
	v_mov_b32_e32 v101, v2
	v_mov_b32_e32 v110, v2
	v_mov_b32_e32 v111, v2
	v_mov_b32_e32 v112, v2
	v_mov_b32_e32 v113, v2
	v_mov_b32_e32 v118, v2
	v_mov_b32_e32 v119, v2
	v_mov_b32_e32 v120, v2
	v_mov_b32_e32 v121, v2
	v_mov_b32_e32 v74, v2
	v_mov_b32_e32 v75, v2
	v_mov_b32_e32 v76, v2
	v_mov_b32_e32 v77, v2
	v_mov_b32_e32 v86, v2
	v_mov_b32_e32 v87, v2
	v_mov_b32_e32 v88, v2
	v_mov_b32_e32 v89, v2
	v_mov_b32_e32 v90, v2
	v_mov_b32_e32 v91, v2
	v_mov_b32_e32 v92, v2
	v_mov_b32_e32 v93, v2
	v_mov_b32_e32 v102, v2
	v_mov_b32_e32 v103, v2
	v_mov_b32_e32 v104, v2
	v_mov_b32_e32 v105, v2
	v_mov_b32_e32 v106, v2
	v_mov_b32_e32 v107, v2
	v_mov_b32_e32 v108, v2
	v_mov_b32_e32 v109, v2
	v_mov_b32_e32 v114, v2
	v_mov_b32_e32 v115, v2
	v_mov_b32_e32 v116, v2
	v_mov_b32_e32 v117, v2
	v_mov_b32_e32 v122, v2
	v_mov_b32_e32 v123, v2
	v_mov_b32_e32 v124, v2
	v_mov_b32_e32 v125, v2
	v_mov_b32_e32 v126, v2
	v_mov_b32_e32 v127, v2
	v_mov_b32_e32 v128, v2
	v_mov_b32_e32 v129, v2
	s_branch .LBB0_434

.LBB0_499:
	v_add_u32_e32 v166, s85, v167
	ds_read_b128 v[130:133], v166
	ds_read_b128 v[134:137], v166 offset:1024
	ds_read_b128 v[158:161], v166 offset:2048
	ds_read_b128 v[186:189], v166 offset:3072
	v_add_u32_e32 v166, s86, v167
	ds_read_b128 v[190:193], v166
	ds_read_b128 v[194:197], v166 offset:1024
	ds_read_b128 v[198:201], v166 offset:2048
	ds_read_b128 v[202:205], v166 offset:3072
	s_add_u32 s30, s34, 0xfffc0080
	s_addc_u32 s31, s35, -1
	s_cmp_eq_u32 s88, 12
	s_cselect_b32 s37, s9, s31
	s_cselect_b32 s36, s25, s30
	s_cselect_b32 s31, s23, s39
	s_cselect_b32 s30, s33, s38
	v_lshl_add_u64 v[238:239], s[34:35], 0, v[150:151]
	s_add_i32 m0, s77, 0xc000
	ds_read_b128 v[206:209], v149
	ds_read_b128 v[210:213], v149 offset:1024
	ds_read_b128 v[214:217], v149 offset:2048
	ds_read_b128 v[218:221], v149 offset:3072
	ds_read_b128 v[222:225], v149 offset:4096
	ds_read_b128 v[226:229], v149 offset:5120
	ds_read_b128 v[230:233], v149 offset:6144
	ds_read_b128 v[234:237], v149 offset:7168
	global_load_lds_dwordx4 v[238:239], off
	v_lshl_add_u64 v[238:239], s[34:35], 0, v[152:153]
	s_add_i32 m0, s77, 0xe000
	s_nop 0
	global_load_lds_dwordx4 v[238:239], off
	s_waitcnt vmcnt(8)
	s_waitcnt lgkmcnt(0)
	s_setprio 1
	s_barrier
	v_mfma_f32_16x16x32_bf16 v[126:129], v[130:133], v[206:209], v[126:129]
	v_mfma_f32_16x16x32_bf16 v[122:125], v[158:161], v[206:209], v[122:125]
	v_mfma_f32_16x16x32_bf16 v[110:113], v[130:133], v[214:217], v[110:113]
	v_mfma_f32_16x16x32_bf16 v[106:109], v[158:161], v[214:217], v[106:109]
	v_mfma_f32_16x16x32_bf16 v[94:97], v[130:133], v[222:225], v[94:97]
	v_mfma_f32_16x16x32_bf16 v[90:93], v[158:161], v[222:225], v[90:93]
	v_mfma_f32_16x16x32_bf16 v[78:81], v[130:133], v[230:233], v[78:81]
	v_mfma_f32_16x16x32_bf16 v[74:77], v[158:161], v[230:233], v[74:77]
	v_mfma_f32_16x16x32_bf16 v[126:129], v[134:137], v[210:213], v[126:129]
	v_mfma_f32_16x16x32_bf16 v[122:125], v[186:189], v[210:213], v[122:125]
	v_mfma_f32_16x16x32_bf16 v[110:113], v[134:137], v[218:221], v[110:113]
	v_mfma_f32_16x16x32_bf16 v[106:109], v[186:189], v[218:221], v[106:109]
	v_mfma_f32_16x16x32_bf16 v[94:97], v[134:137], v[226:229], v[94:97]
	v_mfma_f32_16x16x32_bf16 v[90:93], v[186:189], v[226:229], v[90:93]
	v_mfma_f32_16x16x32_bf16 v[78:81], v[134:137], v[234:237], v[78:81]
	v_mfma_f32_16x16x32_bf16 v[74:77], v[186:189], v[234:237], v[74:77]
	v_mfma_f32_16x16x32_bf16 v[118:121], v[190:193], v[206:209], v[118:121]
	v_mfma_f32_16x16x32_bf16 v[114:117], v[198:201], v[206:209], v[114:117]
	v_mfma_f32_16x16x32_bf16 v[102:105], v[190:193], v[214:217], v[102:105]
	v_mfma_f32_16x16x32_bf16 v[98:101], v[198:201], v[214:217], v[98:101]
	v_mfma_f32_16x16x32_bf16 v[86:89], v[190:193], v[222:225], v[86:89]
	v_mfma_f32_16x16x32_bf16 v[82:85], v[198:201], v[222:225], v[82:85]
	v_mfma_f32_16x16x32_bf16 v[70:73], v[190:193], v[230:233], v[70:73]
	v_mfma_f32_16x16x32_bf16 v[66:69], v[198:201], v[230:233], v[66:69]
	v_mfma_f32_16x16x32_bf16 v[118:121], v[194:197], v[210:213], v[118:121]
	v_mfma_f32_16x16x32_bf16 v[114:117], v[202:205], v[210:213], v[114:117]
	v_mfma_f32_16x16x32_bf16 v[102:105], v[194:197], v[218:221], v[102:105]
	v_mfma_f32_16x16x32_bf16 v[98:101], v[202:205], v[218:221], v[98:101]
	v_mfma_f32_16x16x32_bf16 v[86:89], v[194:197], v[226:229], v[86:89]
	v_mfma_f32_16x16x32_bf16 v[82:85], v[202:205], v[226:229], v[82:85]
	v_mfma_f32_16x16x32_bf16 v[70:73], v[194:197], v[234:237], v[70:73]
	v_mfma_f32_16x16x32_bf16 v[66:69], v[202:205], v[234:237], v[66:69]
	s_barrier
	s_setprio 0
	s_add_i32 s90, s85, s76
	v_lshl_add_u64 v[238:239], s[30:31], 0, v[140:141]
	s_mov_b32 m0, s90
	ds_read_b128 v[206:209], v149 offset:16384
	ds_read_b128 v[210:213], v149 offset:17408
	ds_read_b128 v[214:217], v149 offset:18432
	ds_read_b128 v[218:221], v149 offset:19456
	ds_read_b128 v[222:225], v149 offset:20480
	ds_read_b128 v[226:229], v149 offset:21504
	ds_read_b128 v[230:233], v149 offset:22528
	ds_read_b128 v[234:237], v149 offset:23552
	global_load_lds_dwordx4 v[238:239], off
	s_add_i32 m0, s90, 0x2000
	s_add_u32 s96, s30, 0x40000
	v_lshl_add_u64 v[240:241], s[30:31], 0, v[144:145]
	s_addc_u32 s97, s31, 0
	s_add_i32 s90, s86, s76
	global_load_lds_dwordx4 v[240:241], off
	v_lshl_add_u64 v[242:243], s[96:97], 0, v[140:141]
	s_mov_b32 m0, s90
	v_lshl_add_u64 v[244:245], s[36:37], 0, v[142:143]
	global_load_lds_dwordx4 v[242:243], off
	v_lshl_add_u64 v[242:243], s[96:97], 0, v[144:145]
	s_add_i32 m0, s90, 0x2000
	s_nop 0
	global_load_lds_dwordx4 v[242:243], off
	v_lshl_add_u64 v[242:243], s[36:37], 0, v[138:139]
	s_mov_b32 m0, s77
	s_nop 0
	global_load_lds_dwordx4 v[242:243], off
	s_mov_b32 m0, s78
	s_nop 0
	global_load_lds_dwordx4 v[244:245], off
	s_waitcnt vmcnt(8)
	s_waitcnt lgkmcnt(0)
	s_setprio 1
	s_barrier
	v_mfma_f32_16x16x32_bf16 v[62:65], v[130:133], v[206:209], v[62:65]
	v_mfma_f32_16x16x32_bf16 v[58:61], v[158:161], v[206:209], v[58:61]
	v_mfma_f32_16x16x32_bf16 v[46:49], v[130:133], v[214:217], v[46:49]
	v_mfma_f32_16x16x32_bf16 v[42:45], v[158:161], v[214:217], v[42:45]
	v_mfma_f32_16x16x32_bf16 v[30:33], v[130:133], v[222:225], v[30:33]
	v_mfma_f32_16x16x32_bf16 v[26:29], v[158:161], v[222:225], v[26:29]
	v_mfma_f32_16x16x32_bf16 v[14:17], v[130:133], v[230:233], v[14:17]
	v_mfma_f32_16x16x32_bf16 v[10:13], v[158:161], v[230:233], v[10:13]
	v_mfma_f32_16x16x32_bf16 v[62:65], v[134:137], v[210:213], v[62:65]
	v_mfma_f32_16x16x32_bf16 v[58:61], v[186:189], v[210:213], v[58:61]
	v_mfma_f32_16x16x32_bf16 v[46:49], v[134:137], v[218:221], v[46:49]
	v_mfma_f32_16x16x32_bf16 v[42:45], v[186:189], v[218:221], v[42:45]
	v_mfma_f32_16x16x32_bf16 v[30:33], v[134:137], v[226:229], v[30:33]
	v_mfma_f32_16x16x32_bf16 v[26:29], v[186:189], v[226:229], v[26:29]
	v_mfma_f32_16x16x32_bf16 v[14:17], v[134:137], v[234:237], v[14:17]
	v_mfma_f32_16x16x32_bf16 v[10:13], v[186:189], v[234:237], v[10:13]
	v_mfma_f32_16x16x32_bf16 v[54:57], v[190:193], v[206:209], v[54:57]
	v_mfma_f32_16x16x32_bf16 v[50:53], v[198:201], v[206:209], v[50:53]
	v_mfma_f32_16x16x32_bf16 v[38:41], v[190:193], v[214:217], v[38:41]
	v_mfma_f32_16x16x32_bf16 v[34:37], v[198:201], v[214:217], v[34:37]
	v_mfma_f32_16x16x32_bf16 v[22:25], v[190:193], v[222:225], v[22:25]
	v_mfma_f32_16x16x32_bf16 v[18:21], v[198:201], v[222:225], v[18:21]
	v_mfma_f32_16x16x32_bf16 v[6:9], v[190:193], v[230:233], v[6:9]
	v_mfma_f32_16x16x32_bf16 v[2:5], v[198:201], v[230:233], v[2:5]
	v_mfma_f32_16x16x32_bf16 v[54:57], v[194:197], v[210:213], v[54:57]
	v_mfma_f32_16x16x32_bf16 v[50:53], v[202:205], v[210:213], v[50:53]
	v_mfma_f32_16x16x32_bf16 v[38:41], v[194:197], v[218:221], v[38:41]
	v_mfma_f32_16x16x32_bf16 v[34:37], v[202:205], v[218:221], v[34:37]
	v_mfma_f32_16x16x32_bf16 v[22:25], v[194:197], v[226:229], v[22:25]
	v_mfma_f32_16x16x32_bf16 v[18:21], v[202:205], v[226:229], v[18:21]
	v_mfma_f32_16x16x32_bf16 v[6:9], v[194:197], v[234:237], v[6:9]
	v_mfma_f32_16x16x32_bf16 v[2:5], v[202:205], v[234:237], v[2:5]
	s_barrier
	s_setprio 0
	s_add_i32 s90, 0, 0x18000
	v_add_u32_e32 v166, s90, v167
	s_add_i32 s96, 0, 0x1c000
	ds_read_b128 v[130:133], v166
	ds_read_b128 v[134:137], v166 offset:1024
	ds_read_b128 v[158:161], v166 offset:2048
	ds_read_b128 v[186:189], v166 offset:3072
	v_add_u32_e32 v166, s96, v167
	ds_read_b128 v[190:193], v166
	ds_read_b128 v[194:197], v166 offset:1024
	ds_read_b128 v[198:201], v166 offset:2048
	ds_read_b128 v[202:205], v166 offset:3072
	s_add_u32 s36, s36, 0x40000
	s_addc_u32 s37, s37, 0
	s_mov_b32 m0, s79
	v_lshl_add_u64 v[246:247], s[36:37], 0, v[138:139]
	ds_read_b128 v[206:209], v149 offset:32768
	ds_read_b128 v[210:213], v149 offset:33792
	ds_read_b128 v[214:217], v149 offset:34816
	ds_read_b128 v[218:221], v149 offset:35840
	ds_read_b128 v[222:225], v149 offset:36864
	ds_read_b128 v[226:229], v149 offset:37888
	ds_read_b128 v[230:233], v149 offset:38912
	ds_read_b128 v[234:237], v149 offset:39936
	global_load_lds_dwordx4 v[246:247], off
	v_lshl_add_u64 v[246:247], s[36:37], 0, v[142:143]
	s_mov_b32 m0, s80
	s_nop 0
	global_load_lds_dwordx4 v[246:247], off
	s_waitcnt vmcnt(8)
	s_waitcnt lgkmcnt(0)
	s_setprio 1
	s_barrier
	v_mfma_f32_16x16x32_bf16 v[126:129], v[130:133], v[206:209], v[126:129]
	v_mfma_f32_16x16x32_bf16 v[122:125], v[158:161], v[206:209], v[122:125]
	v_mfma_f32_16x16x32_bf16 v[110:113], v[130:133], v[214:217], v[110:113]
	v_mfma_f32_16x16x32_bf16 v[106:109], v[158:161], v[214:217], v[106:109]
	v_mfma_f32_16x16x32_bf16 v[94:97], v[130:133], v[222:225], v[94:97]
	v_mfma_f32_16x16x32_bf16 v[90:93], v[158:161], v[222:225], v[90:93]
	v_mfma_f32_16x16x32_bf16 v[78:81], v[130:133], v[230:233], v[78:81]
	v_mfma_f32_16x16x32_bf16 v[74:77], v[158:161], v[230:233], v[74:77]
	v_mfma_f32_16x16x32_bf16 v[126:129], v[134:137], v[210:213], v[126:129]
	v_mfma_f32_16x16x32_bf16 v[122:125], v[186:189], v[210:213], v[122:125]
	v_mfma_f32_16x16x32_bf16 v[110:113], v[134:137], v[218:221], v[110:113]
	v_mfma_f32_16x16x32_bf16 v[106:109], v[186:189], v[218:221], v[106:109]
	v_mfma_f32_16x16x32_bf16 v[94:97], v[134:137], v[226:229], v[94:97]
	v_mfma_f32_16x16x32_bf16 v[90:93], v[186:189], v[226:229], v[90:93]
	v_mfma_f32_16x16x32_bf16 v[78:81], v[134:137], v[234:237], v[78:81]
	v_mfma_f32_16x16x32_bf16 v[74:77], v[186:189], v[234:237], v[74:77]
	v_mfma_f32_16x16x32_bf16 v[118:121], v[190:193], v[206:209], v[118:121]
	v_mfma_f32_16x16x32_bf16 v[114:117], v[198:201], v[206:209], v[114:117]
	v_mfma_f32_16x16x32_bf16 v[102:105], v[190:193], v[214:217], v[102:105]
	v_mfma_f32_16x16x32_bf16 v[98:101], v[198:201], v[214:217], v[98:101]
	v_mfma_f32_16x16x32_bf16 v[86:89], v[190:193], v[222:225], v[86:89]
	v_mfma_f32_16x16x32_bf16 v[82:85], v[198:201], v[222:225], v[82:85]
	v_mfma_f32_16x16x32_bf16 v[70:73], v[190:193], v[230:233], v[70:73]
	v_mfma_f32_16x16x32_bf16 v[66:69], v[198:201], v[230:233], v[66:69]
	v_mfma_f32_16x16x32_bf16 v[118:121], v[194:197], v[210:213], v[118:121]
	v_mfma_f32_16x16x32_bf16 v[114:117], v[202:205], v[210:213], v[114:117]
	v_mfma_f32_16x16x32_bf16 v[102:105], v[194:197], v[218:221], v[102:105]
	v_mfma_f32_16x16x32_bf16 v[98:101], v[202:205], v[218:221], v[98:101]
	v_mfma_f32_16x16x32_bf16 v[86:89], v[194:197], v[226:229], v[86:89]
	v_mfma_f32_16x16x32_bf16 v[82:85], v[202:205], v[226:229], v[82:85]
	v_mfma_f32_16x16x32_bf16 v[70:73], v[194:197], v[234:237], v[70:73]
	v_mfma_f32_16x16x32_bf16 v[66:69], v[202:205], v[234:237], v[66:69]
	s_barrier
	s_setprio 0
	s_add_i32 s36, s90, s76
	v_lshl_add_u64 v[238:239], v[238:239], 0, s[18:19]
	s_mov_b32 m0, s36
	ds_read_b128 v[206:209], v149 offset:49152
	ds_read_b128 v[210:213], v149 offset:50176
	ds_read_b128 v[214:217], v149 offset:51200
	ds_read_b128 v[218:221], v149 offset:52224
	ds_read_b128 v[222:225], v149 offset:53248
	ds_read_b128 v[226:229], v149 offset:54272
	ds_read_b128 v[230:233], v149 offset:55296
	ds_read_b128 v[234:237], v149 offset:56320
	global_load_lds_dwordx4 v[238:239], off
	s_add_i32 m0, s36, 0x2000
	s_add_u32 s30, s30, 0x40080
	v_lshl_add_u64 v[238:239], v[240:241], 0, s[18:19]
	s_addc_u32 s31, s31, 0
	s_add_i32 s36, s96, s76
	global_load_lds_dwordx4 v[238:239], off
	v_lshl_add_u64 v[238:239], s[30:31], 0, v[140:141]
	s_mov_b32 m0, s36
	s_nop 0
	global_load_lds_dwordx4 v[238:239], off
	v_lshl_add_u64 v[238:239], s[30:31], 0, v[144:145]
	s_add_i32 m0, s36, 0x2000
	s_nop 0
	global_load_lds_dwordx4 v[238:239], off
	v_lshl_add_u64 v[238:239], v[242:243], 0, s[18:19]
	s_mov_b32 m0, s55
	s_nop 0
	global_load_lds_dwordx4 v[238:239], off
	v_lshl_add_u64 v[238:239], v[244:245], 0, s[18:19]
	s_mov_b32 m0, s81
	s_nop 0
	global_load_lds_dwordx4 v[238:239], off
	s_waitcnt vmcnt(8)
	s_waitcnt lgkmcnt(0)
	s_setprio 1
	s_barrier
	v_mfma_f32_16x16x32_bf16 v[62:65], v[130:133], v[206:209], v[62:65]
	v_mfma_f32_16x16x32_bf16 v[58:61], v[158:161], v[206:209], v[58:61]
	v_mfma_f32_16x16x32_bf16 v[46:49], v[130:133], v[214:217], v[46:49]
	v_mfma_f32_16x16x32_bf16 v[42:45], v[158:161], v[214:217], v[42:45]
	v_mfma_f32_16x16x32_bf16 v[30:33], v[130:133], v[222:225], v[30:33]
	v_mfma_f32_16x16x32_bf16 v[26:29], v[158:161], v[222:225], v[26:29]
	v_mfma_f32_16x16x32_bf16 v[14:17], v[130:133], v[230:233], v[14:17]
	v_mfma_f32_16x16x32_bf16 v[10:13], v[158:161], v[230:233], v[10:13]
	v_mfma_f32_16x16x32_bf16 v[62:65], v[134:137], v[210:213], v[62:65]
	v_mfma_f32_16x16x32_bf16 v[58:61], v[186:189], v[210:213], v[58:61]
	v_mfma_f32_16x16x32_bf16 v[46:49], v[134:137], v[218:221], v[46:49]
	v_mfma_f32_16x16x32_bf16 v[42:45], v[186:189], v[218:221], v[42:45]
	v_mfma_f32_16x16x32_bf16 v[30:33], v[134:137], v[226:229], v[30:33]
	v_mfma_f32_16x16x32_bf16 v[26:29], v[186:189], v[226:229], v[26:29]
	v_mfma_f32_16x16x32_bf16 v[14:17], v[134:137], v[234:237], v[14:17]
	v_mfma_f32_16x16x32_bf16 v[10:13], v[186:189], v[234:237], v[10:13]
	v_mfma_f32_16x16x32_bf16 v[54:57], v[190:193], v[206:209], v[54:57]
	v_mfma_f32_16x16x32_bf16 v[50:53], v[198:201], v[206:209], v[50:53]
	v_mfma_f32_16x16x32_bf16 v[38:41], v[190:193], v[214:217], v[38:41]
	v_mfma_f32_16x16x32_bf16 v[34:37], v[198:201], v[214:217], v[34:37]
	v_mfma_f32_16x16x32_bf16 v[22:25], v[190:193], v[222:225], v[22:25]
	v_mfma_f32_16x16x32_bf16 v[18:21], v[198:201], v[222:225], v[18:21]
	v_mfma_f32_16x16x32_bf16 v[6:9], v[190:193], v[230:233], v[6:9]
	v_mfma_f32_16x16x32_bf16 v[2:5], v[198:201], v[230:233], v[2:5]
	v_mfma_f32_16x16x32_bf16 v[54:57], v[194:197], v[210:213], v[54:57]
	v_mfma_f32_16x16x32_bf16 v[50:53], v[202:205], v[210:213], v[50:53]
	v_mfma_f32_16x16x32_bf16 v[38:41], v[194:197], v[218:221], v[38:41]
	v_mfma_f32_16x16x32_bf16 v[34:37], v[202:205], v[218:221], v[34:37]
	v_mfma_f32_16x16x32_bf16 v[22:25], v[194:197], v[226:229], v[22:25]
	v_mfma_f32_16x16x32_bf16 v[18:21], v[202:205], v[226:229], v[18:21]
	v_mfma_f32_16x16x32_bf16 v[6:9], v[194:197], v[234:237], v[6:9]
	v_mfma_f32_16x16x32_bf16 v[2:5], v[202:205], v[234:237], v[2:5]
	s_barrier
	s_setprio 0
	s_add_i32 s88, s88, 2
	s_add_u32 s34, s34, 0x100
	s_addc_u32 s35, s35, 0
	s_add_u32 s38, s38, 0x100
	s_addc_u32 s39, s39, 0
	s_cmp_gt_u32 s88, 13
	s_cbranch_scc0 .LBB0_499
	s_and_b64 vcc, exec, s[20:21]
	s_cbranch_vccz .LBB0_502
	s_barrier

.LBB0_1720:
	s_or_b32 s18, s87, 1
	v_add_u32_e32 v111, s80, v147
	s_lshl_b64 s[36:37], s[18:19], 7
	s_add_i32 s18, s87, 2
	ds_read_b128 v[150:153], v111
	ds_read_b128 v[154:157], v111 offset:1024
	ds_read_b128 v[158:161], v111 offset:2048
	ds_read_b128 v[162:165], v111 offset:3072
	v_add_u32_e32 v111, s81, v147
	s_lshl_b64 s[38:39], s[18:19], 7
	ds_read_b128 v[168:171], v111
	ds_read_b128 v[172:175], v111 offset:1024
	ds_read_b128 v[176:179], v111 offset:2048
	ds_read_b128 v[180:183], v111 offset:3072
	s_add_u32 s68, s14, s38
	s_addc_u32 s69, s15, s39
	s_and_b64 s[34:35], s[30:31], exec
	s_cselect_b32 s35, s23, s69
	s_cselect_b32 s34, s83, s68
	s_add_u32 s38, s12, s38
	s_addc_u32 s39, s13, s39
	s_and_b64 s[30:31], s[30:31], exec
	s_cselect_b32 s31, s21, s39
	s_cselect_b32 s30, s84, s38
	s_add_u32 s36, s85, s36
	s_addc_u32 s37, s86, s37
	v_lshl_add_u64 v[112:113], s[36:37], 0, v[138:139]
	s_add_i32 m0, s11, 0xc000
	ds_read_b128 v[184:187], v148
	ds_read_b128 v[188:191], v148 offset:1024
	ds_read_b128 v[192:195], v148 offset:2048
	ds_read_b128 v[196:199], v148 offset:3072
	ds_read_b128 v[200:203], v148 offset:4096
	ds_read_b128 v[204:207], v148 offset:5120
	ds_read_b128 v[208:211], v148 offset:6144
	ds_read_b128 v[212:215], v148 offset:7168
	global_load_lds_dwordx4 v[112:113], off
	v_lshl_add_u64 v[112:113], s[36:37], 0, v[140:141]
	s_add_i32 m0, s11, 0xe000
	s_nop 0
	global_load_lds_dwordx4 v[112:113], off
	s_waitcnt vmcnt(8)
	s_waitcnt lgkmcnt(0)
	s_setprio 1
	s_barrier
	v_mfma_f32_16x16x32_bf16 v[130:133], v[150:153], v[184:187], v[130:133]
	v_mfma_f32_16x16x32_bf16 v[126:129], v[158:161], v[184:187], v[126:129]
	v_mfma_f32_16x16x32_bf16 v[112:115], v[150:153], v[192:195], v[114:117]
	v_mfma_f32_16x16x32_bf16 v[106:109], v[158:161], v[192:195], v[106:109]
	v_mfma_f32_16x16x32_bf16 v[94:97], v[150:153], v[200:203], v[94:97]
	v_mfma_f32_16x16x32_bf16 v[90:93], v[158:161], v[200:203], v[90:93]
	v_mfma_f32_16x16x32_bf16 v[78:81], v[150:153], v[208:211], v[78:81]
	v_mfma_f32_16x16x32_bf16 v[74:77], v[158:161], v[208:211], v[74:77]
	v_mfma_f32_16x16x32_bf16 v[130:133], v[154:157], v[188:191], v[130:133]
	v_mfma_f32_16x16x32_bf16 v[126:129], v[162:165], v[188:191], v[126:129]
	v_mfma_f32_16x16x32_bf16 v[112:115], v[154:157], v[196:199], v[112:115]
	v_mfma_f32_16x16x32_bf16 v[106:109], v[162:165], v[196:199], v[106:109]
	v_mfma_f32_16x16x32_bf16 v[94:97], v[154:157], v[204:207], v[94:97]
	v_mfma_f32_16x16x32_bf16 v[90:93], v[162:165], v[204:207], v[90:93]
	v_mfma_f32_16x16x32_bf16 v[78:81], v[154:157], v[212:215], v[78:81]
	v_mfma_f32_16x16x32_bf16 v[74:77], v[162:165], v[212:215], v[74:77]
	v_mfma_f32_16x16x32_bf16 v[122:125], v[168:171], v[184:187], v[122:125]
	v_mfma_f32_16x16x32_bf16 v[116:119], v[176:179], v[184:187], v[118:121]
	v_mfma_f32_16x16x32_bf16 v[102:105], v[168:171], v[192:195], v[102:105]
	v_mfma_f32_16x16x32_bf16 v[98:101], v[176:179], v[192:195], v[98:101]
	v_mfma_f32_16x16x32_bf16 v[86:89], v[168:171], v[200:203], v[86:89]
	v_mfma_f32_16x16x32_bf16 v[82:85], v[176:179], v[200:203], v[82:85]
	v_mfma_f32_16x16x32_bf16 v[70:73], v[168:171], v[208:211], v[70:73]
	v_mfma_f32_16x16x32_bf16 v[66:69], v[176:179], v[208:211], v[66:69]
	v_mfma_f32_16x16x32_bf16 v[122:125], v[172:175], v[188:191], v[122:125]
	v_mfma_f32_16x16x32_bf16 v[118:121], v[180:183], v[188:191], v[116:119]
	v_mfma_f32_16x16x32_bf16 v[102:105], v[172:175], v[196:199], v[102:105]
	v_mfma_f32_16x16x32_bf16 v[98:101], v[180:183], v[196:199], v[98:101]
	v_mfma_f32_16x16x32_bf16 v[86:89], v[172:175], v[204:207], v[86:89]
	v_mfma_f32_16x16x32_bf16 v[82:85], v[180:183], v[204:207], v[82:85]
	v_mfma_f32_16x16x32_bf16 v[70:73], v[172:175], v[212:215], v[70:73]
	v_mfma_f32_16x16x32_bf16 v[66:69], v[180:183], v[212:215], v[66:69]
	s_barrier
	s_setprio 0
	s_add_i32 s36, s80, s73
	v_lshl_add_u64 v[216:217], s[30:31], 0, v[134:135]
	s_mov_b32 m0, s36
	ds_read_b128 v[184:187], v148 offset:16384
	ds_read_b128 v[188:191], v148 offset:17408
	ds_read_b128 v[192:195], v148 offset:18432
	ds_read_b128 v[196:199], v148 offset:19456
	ds_read_b128 v[200:203], v148 offset:20480
	ds_read_b128 v[204:207], v148 offset:21504
	ds_read_b128 v[208:211], v148 offset:22528
	ds_read_b128 v[212:215], v148 offset:23552
	global_load_lds_dwordx4 v[216:217], off
	s_add_i32 m0, s36, 0x2000
	s_add_u32 s36, s30, 0x40000
	v_lshl_add_u64 v[218:219], s[30:31], 0, v[136:137]
	s_addc_u32 s37, s31, 0
	s_add_i32 s38, s81, s73
	global_load_lds_dwordx4 v[218:219], off
	v_lshl_add_u64 v[116:117], s[36:37], 0, v[134:135]
	s_mov_b32 m0, s38
	v_lshl_add_u64 v[220:221], s[34:35], 0, v[138:139]
	global_load_lds_dwordx4 v[116:117], off
	v_lshl_add_u64 v[116:117], s[36:37], 0, v[136:137]
	s_add_i32 m0, s38, 0x2000
	v_lshl_add_u64 v[222:223], s[34:35], 0, v[140:141]
	global_load_lds_dwordx4 v[116:117], off
	s_mov_b32 m0, s11
	s_nop 0
	global_load_lds_dwordx4 v[220:221], off
	s_mov_b32 m0, s74
	s_nop 0
	global_load_lds_dwordx4 v[222:223], off
	s_waitcnt vmcnt(8)
	s_waitcnt lgkmcnt(0)
	s_setprio 1
	s_barrier
	v_mfma_f32_16x16x32_bf16 v[62:65], v[150:153], v[184:187], v[62:65]
	v_mfma_f32_16x16x32_bf16 v[58:61], v[158:161], v[184:187], v[58:61]
	v_mfma_f32_16x16x32_bf16 v[46:49], v[150:153], v[192:195], v[46:49]
	v_mfma_f32_16x16x32_bf16 v[42:45], v[158:161], v[192:195], v[42:45]
	v_mfma_f32_16x16x32_bf16 v[30:33], v[150:153], v[200:203], v[30:33]
	v_mfma_f32_16x16x32_bf16 v[26:29], v[158:161], v[200:203], v[26:29]
	v_mfma_f32_16x16x32_bf16 v[14:17], v[150:153], v[208:211], v[14:17]
	v_mfma_f32_16x16x32_bf16 v[10:13], v[158:161], v[208:211], v[10:13]
	v_mfma_f32_16x16x32_bf16 v[62:65], v[154:157], v[188:191], v[62:65]
	v_mfma_f32_16x16x32_bf16 v[58:61], v[162:165], v[188:191], v[58:61]
	v_mfma_f32_16x16x32_bf16 v[46:49], v[154:157], v[196:199], v[46:49]
	v_mfma_f32_16x16x32_bf16 v[42:45], v[162:165], v[196:199], v[42:45]
	v_mfma_f32_16x16x32_bf16 v[30:33], v[154:157], v[204:207], v[30:33]
	v_mfma_f32_16x16x32_bf16 v[26:29], v[162:165], v[204:207], v[26:29]
	v_mfma_f32_16x16x32_bf16 v[14:17], v[154:157], v[212:215], v[14:17]
	v_mfma_f32_16x16x32_bf16 v[10:13], v[162:165], v[212:215], v[10:13]
	v_mfma_f32_16x16x32_bf16 v[54:57], v[168:171], v[184:187], v[54:57]
	v_mfma_f32_16x16x32_bf16 v[50:53], v[176:179], v[184:187], v[50:53]
	v_mfma_f32_16x16x32_bf16 v[38:41], v[168:171], v[192:195], v[38:41]
	v_mfma_f32_16x16x32_bf16 v[34:37], v[176:179], v[192:195], v[34:37]
	v_mfma_f32_16x16x32_bf16 v[22:25], v[168:171], v[200:203], v[22:25]
	v_mfma_f32_16x16x32_bf16 v[18:21], v[176:179], v[200:203], v[18:21]
	v_mfma_f32_16x16x32_bf16 v[6:9], v[168:171], v[208:211], v[6:9]
	v_mfma_f32_16x16x32_bf16 v[2:5], v[176:179], v[208:211], v[2:5]
	v_mfma_f32_16x16x32_bf16 v[54:57], v[172:175], v[188:191], v[54:57]
	v_mfma_f32_16x16x32_bf16 v[50:53], v[180:183], v[188:191], v[50:53]
	v_mfma_f32_16x16x32_bf16 v[38:41], v[172:175], v[196:199], v[38:41]
	v_mfma_f32_16x16x32_bf16 v[34:37], v[180:183], v[196:199], v[34:37]
	v_mfma_f32_16x16x32_bf16 v[22:25], v[172:175], v[204:207], v[22:25]
	v_mfma_f32_16x16x32_bf16 v[18:21], v[180:183], v[204:207], v[18:21]
	v_mfma_f32_16x16x32_bf16 v[6:9], v[172:175], v[212:215], v[6:9]
	v_mfma_f32_16x16x32_bf16 v[2:5], v[180:183], v[212:215], v[2:5]
	s_barrier
	s_setprio 0
	s_add_i32 s36, 0, 0x18000
	v_add_u32_e32 v111, s36, v147
	s_add_i32 s37, 0, 0x1c000
	ds_read_b128 v[150:153], v111
	ds_read_b128 v[154:157], v111 offset:1024
	ds_read_b128 v[158:161], v111 offset:2048
	ds_read_b128 v[162:165], v111 offset:3072
	v_add_u32_e32 v111, s37, v147
	ds_read_b128 v[168:171], v111
	ds_read_b128 v[172:175], v111 offset:1024
	ds_read_b128 v[176:179], v111 offset:2048
	ds_read_b128 v[180:183], v111 offset:3072
	s_add_u32 s34, s34, 0x40000
	s_addc_u32 s35, s35, 0
	s_mov_b32 m0, s75
	v_lshl_add_u64 v[116:117], s[34:35], 0, v[138:139]
	ds_read_b128 v[184:187], v148 offset:32768
	ds_read_b128 v[188:191], v148 offset:33792
	ds_read_b128 v[192:195], v148 offset:34816
	ds_read_b128 v[196:199], v148 offset:35840
	ds_read_b128 v[200:203], v148 offset:36864
	ds_read_b128 v[204:207], v148 offset:37888
	ds_read_b128 v[208:211], v148 offset:38912
	ds_read_b128 v[212:215], v148 offset:39936
	global_load_lds_dwordx4 v[116:117], off
	v_lshl_add_u64 v[116:117], s[34:35], 0, v[140:141]
	s_mov_b32 m0, s77
	s_nop 0
	global_load_lds_dwordx4 v[116:117], off
	s_waitcnt vmcnt(8)
	s_waitcnt lgkmcnt(0)
	s_setprio 1
	s_barrier
	v_mfma_f32_16x16x32_bf16 v[130:133], v[150:153], v[184:187], v[130:133]
	v_mfma_f32_16x16x32_bf16 v[126:129], v[158:161], v[184:187], v[126:129]
	v_mfma_f32_16x16x32_bf16 v[112:115], v[150:153], v[192:195], v[112:115]
	v_mfma_f32_16x16x32_bf16 v[106:109], v[158:161], v[192:195], v[106:109]
	v_mfma_f32_16x16x32_bf16 v[94:97], v[150:153], v[200:203], v[94:97]
	v_mfma_f32_16x16x32_bf16 v[90:93], v[158:161], v[200:203], v[90:93]
	v_mfma_f32_16x16x32_bf16 v[78:81], v[150:153], v[208:211], v[78:81]
	v_mfma_f32_16x16x32_bf16 v[74:77], v[158:161], v[208:211], v[74:77]
	v_mfma_f32_16x16x32_bf16 v[130:133], v[154:157], v[188:191], v[130:133]
	v_mfma_f32_16x16x32_bf16 v[126:129], v[162:165], v[188:191], v[126:129]
	v_mfma_f32_16x16x32_bf16 v[114:117], v[154:157], v[196:199], v[112:115]
	v_mfma_f32_16x16x32_bf16 v[106:109], v[162:165], v[196:199], v[106:109]
	v_mfma_f32_16x16x32_bf16 v[94:97], v[154:157], v[204:207], v[94:97]
	v_mfma_f32_16x16x32_bf16 v[90:93], v[162:165], v[204:207], v[90:93]
	v_mfma_f32_16x16x32_bf16 v[78:81], v[154:157], v[212:215], v[78:81]
	v_mfma_f32_16x16x32_bf16 v[74:77], v[162:165], v[212:215], v[74:77]
	v_mfma_f32_16x16x32_bf16 v[122:125], v[168:171], v[184:187], v[122:125]
	v_mfma_f32_16x16x32_bf16 v[118:121], v[176:179], v[184:187], v[118:121]
	v_mfma_f32_16x16x32_bf16 v[102:105], v[168:171], v[192:195], v[102:105]
	v_mfma_f32_16x16x32_bf16 v[98:101], v[176:179], v[192:195], v[98:101]
	v_mfma_f32_16x16x32_bf16 v[86:89], v[168:171], v[200:203], v[86:89]
	v_mfma_f32_16x16x32_bf16 v[82:85], v[176:179], v[200:203], v[82:85]
	v_mfma_f32_16x16x32_bf16 v[70:73], v[168:171], v[208:211], v[70:73]
	v_mfma_f32_16x16x32_bf16 v[66:69], v[176:179], v[208:211], v[66:69]
	v_mfma_f32_16x16x32_bf16 v[122:125], v[172:175], v[188:191], v[122:125]
	v_mfma_f32_16x16x32_bf16 v[118:121], v[180:183], v[188:191], v[118:121]
	v_mfma_f32_16x16x32_bf16 v[102:105], v[172:175], v[196:199], v[102:105]
	v_mfma_f32_16x16x32_bf16 v[98:101], v[180:183], v[196:199], v[98:101]
	v_mfma_f32_16x16x32_bf16 v[86:89], v[172:175], v[204:207], v[86:89]
	v_mfma_f32_16x16x32_bf16 v[82:85], v[180:183], v[204:207], v[82:85]
	v_mfma_f32_16x16x32_bf16 v[70:73], v[172:175], v[212:215], v[70:73]
	v_mfma_f32_16x16x32_bf16 v[66:69], v[180:183], v[212:215], v[66:69]
	s_barrier
	s_setprio 0
	s_add_i32 s34, s36, s73
	v_lshl_add_u64 v[112:113], v[216:217], 0, s[16:17]
	s_mov_b32 m0, s34
	ds_read_b128 v[184:187], v148 offset:49152
	ds_read_b128 v[188:191], v148 offset:50176
	ds_read_b128 v[192:195], v148 offset:51200
	ds_read_b128 v[196:199], v148 offset:52224
	ds_read_b128 v[200:203], v148 offset:53248
	ds_read_b128 v[204:207], v148 offset:54272
	ds_read_b128 v[208:211], v148 offset:55296
	ds_read_b128 v[212:215], v148 offset:56320
	global_load_lds_dwordx4 v[112:113], off
	s_add_i32 m0, s34, 0x2000
	s_add_u32 s30, s30, 0x40080
	v_lshl_add_u64 v[112:113], v[218:219], 0, s[16:17]
	s_addc_u32 s31, s31, 0
	s_add_i32 s34, s37, s73
	global_load_lds_dwordx4 v[112:113], off
	v_lshl_add_u64 v[112:113], s[30:31], 0, v[134:135]
	s_mov_b32 m0, s34
	s_nop 0
	global_load_lds_dwordx4 v[112:113], off
	v_lshl_add_u64 v[112:113], s[30:31], 0, v[136:137]
	s_add_i32 m0, s34, 0x2000
	s_nop 0
	global_load_lds_dwordx4 v[112:113], off
	v_lshl_add_u64 v[112:113], v[220:221], 0, s[16:17]
	s_mov_b32 m0, s78
	s_nop 0
	global_load_lds_dwordx4 v[112:113], off
	v_lshl_add_u64 v[112:113], v[222:223], 0, s[16:17]
	s_mov_b32 m0, s79
	s_nop 0
	global_load_lds_dwordx4 v[112:113], off
	s_waitcnt vmcnt(8)
	s_waitcnt lgkmcnt(0)
	s_setprio 1
	s_barrier
	v_mfma_f32_16x16x32_bf16 v[62:65], v[150:153], v[184:187], v[62:65]
	v_mfma_f32_16x16x32_bf16 v[58:61], v[158:161], v[184:187], v[58:61]
	v_mfma_f32_16x16x32_bf16 v[46:49], v[150:153], v[192:195], v[46:49]
	v_mfma_f32_16x16x32_bf16 v[42:45], v[158:161], v[192:195], v[42:45]
	v_mfma_f32_16x16x32_bf16 v[30:33], v[150:153], v[200:203], v[30:33]
	v_mfma_f32_16x16x32_bf16 v[26:29], v[158:161], v[200:203], v[26:29]
	v_mfma_f32_16x16x32_bf16 v[14:17], v[150:153], v[208:211], v[14:17]
	v_mfma_f32_16x16x32_bf16 v[10:13], v[158:161], v[208:211], v[10:13]
	v_mfma_f32_16x16x32_bf16 v[62:65], v[154:157], v[188:191], v[62:65]
	v_mfma_f32_16x16x32_bf16 v[58:61], v[162:165], v[188:191], v[58:61]
	v_mfma_f32_16x16x32_bf16 v[46:49], v[154:157], v[196:199], v[46:49]
	v_mfma_f32_16x16x32_bf16 v[42:45], v[162:165], v[196:199], v[42:45]
	v_mfma_f32_16x16x32_bf16 v[30:33], v[154:157], v[204:207], v[30:33]
	v_mfma_f32_16x16x32_bf16 v[26:29], v[162:165], v[204:207], v[26:29]
	v_mfma_f32_16x16x32_bf16 v[14:17], v[154:157], v[212:215], v[14:17]
	v_mfma_f32_16x16x32_bf16 v[10:13], v[162:165], v[212:215], v[10:13]
	v_mfma_f32_16x16x32_bf16 v[54:57], v[168:171], v[184:187], v[54:57]
	v_mfma_f32_16x16x32_bf16 v[50:53], v[176:179], v[184:187], v[50:53]
	v_mfma_f32_16x16x32_bf16 v[38:41], v[168:171], v[192:195], v[38:41]
	v_mfma_f32_16x16x32_bf16 v[34:37], v[176:179], v[192:195], v[34:37]
	v_mfma_f32_16x16x32_bf16 v[22:25], v[168:171], v[200:203], v[22:25]
	v_mfma_f32_16x16x32_bf16 v[18:21], v[176:179], v[200:203], v[18:21]
	v_mfma_f32_16x16x32_bf16 v[6:9], v[168:171], v[208:211], v[6:9]
	v_mfma_f32_16x16x32_bf16 v[2:5], v[176:179], v[208:211], v[2:5]
	v_mfma_f32_16x16x32_bf16 v[54:57], v[172:175], v[188:191], v[54:57]
	v_mfma_f32_16x16x32_bf16 v[50:53], v[180:183], v[188:191], v[50:53]
	v_mfma_f32_16x16x32_bf16 v[38:41], v[172:175], v[196:199], v[38:41]
	v_mfma_f32_16x16x32_bf16 v[34:37], v[180:183], v[196:199], v[34:37]
	v_mfma_f32_16x16x32_bf16 v[22:25], v[172:175], v[204:207], v[22:25]
	v_mfma_f32_16x16x32_bf16 v[18:21], v[180:183], v[204:207], v[18:21]
	v_mfma_f32_16x16x32_bf16 v[6:9], v[172:175], v[212:215], v[6:9]
	v_mfma_f32_16x16x32_bf16 v[2:5], v[180:183], v[212:215], v[2:5]
	s_barrier
	s_setprio 0
	s_cmp_gt_u32 s87, 13
	s_cbranch_scc1 .LBB0_1722
	s_mov_b32 s87, s18
	s_branch .LBB0_1705

.LBB0_1888:
	s_lshl_b32 s74, s95, 7
	s_add_u32 s75, s38, s74
	s_addc_u32 s76, s39, 0
	v_add_u32_e32 v142, s87, v144
	s_add_u32 s77, s75, 0x100
	ds_read_b128 v[148:151], v142
	ds_read_b128 v[152:155], v142 offset:1024
	ds_read_b128 v[156:159], v142 offset:2048
	ds_read_b128 v[160:163], v142 offset:3072
	v_add_u32_e32 v142, s88, v144
	s_addc_u32 s78, s76, 0
	ds_read_b128 v[164:167], v142
	ds_read_b128 v[168:171], v142 offset:1024
	ds_read_b128 v[172:175], v142 offset:2048
	ds_read_b128 v[176:179], v142 offset:3072
	s_and_b64 s[72:73], s[70:71], exec
	s_cselect_b32 s73, s25, s78
	s_cselect_b32 s72, s33, s77
	s_add_u32 s74, s36, s74
	s_addc_u32 s77, s37, 0
	s_add_u32 s74, s74, 0x100
	s_addc_u32 s77, s77, 0
	s_and_b64 s[70:71], s[70:71], exec
	s_cselect_b32 s71, s23, s77
	s_cselect_b32 s70, s94, s74
	s_add_u32 s74, s75, 0x40080
	s_addc_u32 s75, s76, 0
	v_lshl_add_u64 v[142:143], s[74:75], 0, v[134:135]
	s_add_i32 m0, s31, 0xc000
	ds_read_b128 v[180:183], v147
	ds_read_b128 v[184:187], v147 offset:1024
	ds_read_b128 v[188:191], v147 offset:2048
	ds_read_b128 v[192:195], v147 offset:3072
	ds_read_b128 v[196:199], v147 offset:4096
	ds_read_b128 v[200:203], v147 offset:5120
	ds_read_b128 v[204:207], v147 offset:6144
	ds_read_b128 v[208:211], v147 offset:7168
	global_load_lds_dwordx4 v[142:143], off
	v_lshl_add_u64 v[142:143], s[74:75], 0, v[136:137]
	s_add_i32 m0, s31, 0xe000
	s_nop 0
	global_load_lds_dwordx4 v[142:143], off
	s_waitcnt vmcnt(8)
	s_waitcnt lgkmcnt(0)
	s_setprio 1
	s_barrier
	v_mfma_f32_16x16x32_bf16 v[126:129], v[148:151], v[180:183], v[126:129]
	v_mfma_f32_16x16x32_bf16 v[122:125], v[156:159], v[180:183], v[122:125]
	v_mfma_f32_16x16x32_bf16 v[110:113], v[148:151], v[188:191], v[110:113]
	v_mfma_f32_16x16x32_bf16 v[106:109], v[156:159], v[188:191], v[106:109]
	v_mfma_f32_16x16x32_bf16 v[94:97], v[148:151], v[196:199], v[94:97]
	v_mfma_f32_16x16x32_bf16 v[90:93], v[156:159], v[196:199], v[90:93]
	v_mfma_f32_16x16x32_bf16 v[78:81], v[148:151], v[204:207], v[78:81]
	v_mfma_f32_16x16x32_bf16 v[74:77], v[156:159], v[204:207], v[74:77]
	v_mfma_f32_16x16x32_bf16 v[126:129], v[152:155], v[184:187], v[126:129]
	v_mfma_f32_16x16x32_bf16 v[122:125], v[160:163], v[184:187], v[122:125]
	v_mfma_f32_16x16x32_bf16 v[110:113], v[152:155], v[192:195], v[110:113]
	v_mfma_f32_16x16x32_bf16 v[106:109], v[160:163], v[192:195], v[106:109]
	v_mfma_f32_16x16x32_bf16 v[94:97], v[152:155], v[200:203], v[94:97]
	v_mfma_f32_16x16x32_bf16 v[90:93], v[160:163], v[200:203], v[90:93]
	v_mfma_f32_16x16x32_bf16 v[78:81], v[152:155], v[208:211], v[78:81]
	v_mfma_f32_16x16x32_bf16 v[74:77], v[160:163], v[208:211], v[74:77]
	v_mfma_f32_16x16x32_bf16 v[118:121], v[164:167], v[180:183], v[118:121]
	v_mfma_f32_16x16x32_bf16 v[114:117], v[172:175], v[180:183], v[114:117]
	v_mfma_f32_16x16x32_bf16 v[102:105], v[164:167], v[188:191], v[102:105]
	v_mfma_f32_16x16x32_bf16 v[98:101], v[172:175], v[188:191], v[98:101]
	v_mfma_f32_16x16x32_bf16 v[86:89], v[164:167], v[196:199], v[86:89]
	v_mfma_f32_16x16x32_bf16 v[82:85], v[172:175], v[196:199], v[82:85]
	v_mfma_f32_16x16x32_bf16 v[70:73], v[164:167], v[204:207], v[70:73]
	v_mfma_f32_16x16x32_bf16 v[66:69], v[172:175], v[204:207], v[66:69]
	v_mfma_f32_16x16x32_bf16 v[118:121], v[168:171], v[184:187], v[118:121]
	v_mfma_f32_16x16x32_bf16 v[114:117], v[176:179], v[184:187], v[114:117]
	v_mfma_f32_16x16x32_bf16 v[102:105], v[168:171], v[192:195], v[102:105]
	v_mfma_f32_16x16x32_bf16 v[98:101], v[176:179], v[192:195], v[98:101]
	v_mfma_f32_16x16x32_bf16 v[86:89], v[168:171], v[200:203], v[86:89]
	v_mfma_f32_16x16x32_bf16 v[82:85], v[176:179], v[200:203], v[82:85]
	v_mfma_f32_16x16x32_bf16 v[70:73], v[168:171], v[208:211], v[70:73]
	v_mfma_f32_16x16x32_bf16 v[66:69], v[176:179], v[208:211], v[66:69]
	s_barrier
	s_setprio 0
	s_add_i32 s74, s87, s49
	v_lshl_add_u64 v[142:143], s[70:71], 0, v[130:131]
	s_mov_b32 m0, s74
	ds_read_b128 v[180:183], v147 offset:16384
	ds_read_b128 v[184:187], v147 offset:17408
	ds_read_b128 v[188:191], v147 offset:18432
	ds_read_b128 v[192:195], v147 offset:19456
	ds_read_b128 v[196:199], v147 offset:20480
	ds_read_b128 v[200:203], v147 offset:21504
	ds_read_b128 v[204:207], v147 offset:22528
	ds_read_b128 v[208:211], v147 offset:23552
	global_load_lds_dwordx4 v[142:143], off
	s_add_i32 m0, s74, 0x2000
	s_add_u32 s74, s70, 0x40000
	v_lshl_add_u64 v[212:213], s[70:71], 0, v[132:133]
	s_addc_u32 s75, s71, 0
	s_add_i32 s76, s88, s49
	global_load_lds_dwordx4 v[212:213], off
	v_lshl_add_u64 v[214:215], s[74:75], 0, v[130:131]
	s_mov_b32 m0, s76
	v_lshl_add_u64 v[216:217], s[72:73], 0, v[136:137]
	global_load_lds_dwordx4 v[214:215], off
	v_lshl_add_u64 v[214:215], s[74:75], 0, v[132:133]
	s_add_i32 m0, s76, 0x2000
	s_nop 0
	global_load_lds_dwordx4 v[214:215], off
	v_lshl_add_u64 v[214:215], s[72:73], 0, v[134:135]
	s_mov_b32 m0, s31
	s_nop 0
	global_load_lds_dwordx4 v[214:215], off
	s_mov_b32 m0, s35
	s_nop 0
	global_load_lds_dwordx4 v[216:217], off
	s_waitcnt vmcnt(8)
	s_waitcnt lgkmcnt(0)
	s_setprio 1
	s_barrier
	v_mfma_f32_16x16x32_bf16 v[62:65], v[148:151], v[180:183], v[62:65]
	v_mfma_f32_16x16x32_bf16 v[58:61], v[156:159], v[180:183], v[58:61]
	v_mfma_f32_16x16x32_bf16 v[46:49], v[148:151], v[188:191], v[46:49]
	v_mfma_f32_16x16x32_bf16 v[42:45], v[156:159], v[188:191], v[42:45]
	v_mfma_f32_16x16x32_bf16 v[30:33], v[148:151], v[196:199], v[30:33]
	v_mfma_f32_16x16x32_bf16 v[26:29], v[156:159], v[196:199], v[26:29]
	v_mfma_f32_16x16x32_bf16 v[14:17], v[148:151], v[204:207], v[14:17]
	v_mfma_f32_16x16x32_bf16 v[10:13], v[156:159], v[204:207], v[10:13]
	v_mfma_f32_16x16x32_bf16 v[62:65], v[152:155], v[184:187], v[62:65]
	v_mfma_f32_16x16x32_bf16 v[58:61], v[160:163], v[184:187], v[58:61]
	v_mfma_f32_16x16x32_bf16 v[46:49], v[152:155], v[192:195], v[46:49]
	v_mfma_f32_16x16x32_bf16 v[42:45], v[160:163], v[192:195], v[42:45]
	v_mfma_f32_16x16x32_bf16 v[30:33], v[152:155], v[200:203], v[30:33]
	v_mfma_f32_16x16x32_bf16 v[26:29], v[160:163], v[200:203], v[26:29]
	v_mfma_f32_16x16x32_bf16 v[14:17], v[152:155], v[208:211], v[14:17]
	v_mfma_f32_16x16x32_bf16 v[10:13], v[160:163], v[208:211], v[10:13]
	v_mfma_f32_16x16x32_bf16 v[54:57], v[164:167], v[180:183], v[54:57]
	v_mfma_f32_16x16x32_bf16 v[50:53], v[172:175], v[180:183], v[50:53]
	v_mfma_f32_16x16x32_bf16 v[38:41], v[164:167], v[188:191], v[38:41]
	v_mfma_f32_16x16x32_bf16 v[34:37], v[172:175], v[188:191], v[34:37]
	v_mfma_f32_16x16x32_bf16 v[22:25], v[164:167], v[196:199], v[22:25]
	v_mfma_f32_16x16x32_bf16 v[18:21], v[172:175], v[196:199], v[18:21]
	v_mfma_f32_16x16x32_bf16 v[6:9], v[164:167], v[204:207], v[6:9]
	v_mfma_f32_16x16x32_bf16 v[2:5], v[172:175], v[204:207], v[2:5]
	v_mfma_f32_16x16x32_bf16 v[54:57], v[168:171], v[184:187], v[54:57]
	v_mfma_f32_16x16x32_bf16 v[50:53], v[176:179], v[184:187], v[50:53]
	v_mfma_f32_16x16x32_bf16 v[38:41], v[168:171], v[192:195], v[38:41]
	v_mfma_f32_16x16x32_bf16 v[34:37], v[176:179], v[192:195], v[34:37]
	v_mfma_f32_16x16x32_bf16 v[22:25], v[168:171], v[200:203], v[22:25]
	v_mfma_f32_16x16x32_bf16 v[18:21], v[176:179], v[200:203], v[18:21]
	v_mfma_f32_16x16x32_bf16 v[6:9], v[168:171], v[208:211], v[6:9]
	v_mfma_f32_16x16x32_bf16 v[2:5], v[176:179], v[208:211], v[2:5]
	s_barrier
	s_setprio 0
	s_add_i32 s74, 0, 0x18000
	s_add_i32 s75, 0, 0x1c000
	v_add_u32_e32 v160, s74, v144
	v_add_u32_e32 v176, s75, v144
	ds_read_b128 v[148:151], v160
	ds_read_b128 v[152:155], v160 offset:1024
	ds_read_b128 v[156:159], v160 offset:2048
	ds_read_b128 v[160:163], v160 offset:3072
	ds_read_b128 v[164:167], v176
	ds_read_b128 v[168:171], v176 offset:1024
	ds_read_b128 v[172:175], v176 offset:2048
	ds_read_b128 v[176:179], v176 offset:3072
	s_add_u32 s72, s72, 0x40000
	s_addc_u32 s73, s73, 0
	s_mov_b32 m0, s81
	v_lshl_add_u64 v[218:219], s[72:73], 0, v[134:135]
	ds_read_b128 v[180:183], v147 offset:32768
	ds_read_b128 v[184:187], v147 offset:33792
	ds_read_b128 v[188:191], v147 offset:34816
	ds_read_b128 v[192:195], v147 offset:35840
	ds_read_b128 v[196:199], v147 offset:36864
	ds_read_b128 v[200:203], v147 offset:37888
	ds_read_b128 v[204:207], v147 offset:38912
	ds_read_b128 v[208:211], v147 offset:39936
	global_load_lds_dwordx4 v[218:219], off
	v_lshl_add_u64 v[218:219], s[72:73], 0, v[136:137]
	s_mov_b32 m0, s82
	s_nop 0
	global_load_lds_dwordx4 v[218:219], off
	s_waitcnt vmcnt(8)
	s_waitcnt lgkmcnt(0)
	s_setprio 1
	s_barrier
	v_mfma_f32_16x16x32_bf16 v[126:129], v[148:151], v[180:183], v[126:129]
	v_mfma_f32_16x16x32_bf16 v[122:125], v[156:159], v[180:183], v[122:125]
	v_mfma_f32_16x16x32_bf16 v[110:113], v[148:151], v[188:191], v[110:113]
	v_mfma_f32_16x16x32_bf16 v[106:109], v[156:159], v[188:191], v[106:109]
	v_mfma_f32_16x16x32_bf16 v[94:97], v[148:151], v[196:199], v[94:97]
	v_mfma_f32_16x16x32_bf16 v[90:93], v[156:159], v[196:199], v[90:93]
	v_mfma_f32_16x16x32_bf16 v[78:81], v[148:151], v[204:207], v[78:81]
	v_mfma_f32_16x16x32_bf16 v[74:77], v[156:159], v[204:207], v[74:77]
	v_mfma_f32_16x16x32_bf16 v[126:129], v[152:155], v[184:187], v[126:129]
	v_mfma_f32_16x16x32_bf16 v[122:125], v[160:163], v[184:187], v[122:125]
	v_mfma_f32_16x16x32_bf16 v[110:113], v[152:155], v[192:195], v[110:113]
	v_mfma_f32_16x16x32_bf16 v[106:109], v[160:163], v[192:195], v[106:109]
	v_mfma_f32_16x16x32_bf16 v[94:97], v[152:155], v[200:203], v[94:97]
	v_mfma_f32_16x16x32_bf16 v[90:93], v[160:163], v[200:203], v[90:93]
	v_mfma_f32_16x16x32_bf16 v[78:81], v[152:155], v[208:211], v[78:81]
	v_mfma_f32_16x16x32_bf16 v[74:77], v[160:163], v[208:211], v[74:77]
	v_mfma_f32_16x16x32_bf16 v[118:121], v[164:167], v[180:183], v[118:121]
	v_mfma_f32_16x16x32_bf16 v[114:117], v[172:175], v[180:183], v[114:117]
	v_mfma_f32_16x16x32_bf16 v[102:105], v[164:167], v[188:191], v[102:105]
	v_mfma_f32_16x16x32_bf16 v[98:101], v[172:175], v[188:191], v[98:101]
	v_mfma_f32_16x16x32_bf16 v[86:89], v[164:167], v[196:199], v[86:89]
	v_mfma_f32_16x16x32_bf16 v[82:85], v[172:175], v[196:199], v[82:85]
	v_mfma_f32_16x16x32_bf16 v[70:73], v[164:167], v[204:207], v[70:73]
	v_mfma_f32_16x16x32_bf16 v[66:69], v[172:175], v[204:207], v[66:69]
	v_mfma_f32_16x16x32_bf16 v[118:121], v[168:171], v[184:187], v[118:121]
	v_mfma_f32_16x16x32_bf16 v[114:117], v[176:179], v[184:187], v[114:117]
	v_mfma_f32_16x16x32_bf16 v[102:105], v[168:171], v[192:195], v[102:105]
	v_mfma_f32_16x16x32_bf16 v[98:101], v[176:179], v[192:195], v[98:101]
	v_mfma_f32_16x16x32_bf16 v[86:89], v[168:171], v[200:203], v[86:89]
	v_mfma_f32_16x16x32_bf16 v[82:85], v[176:179], v[200:203], v[82:85]
	v_mfma_f32_16x16x32_bf16 v[70:73], v[168:171], v[208:211], v[70:73]
	v_mfma_f32_16x16x32_bf16 v[66:69], v[176:179], v[208:211], v[66:69]
	s_barrier
	s_setprio 0
	s_add_i32 s72, s74, s49
	v_lshl_add_u64 v[142:143], v[142:143], 0, s[12:13]
	s_mov_b32 m0, s72
	ds_read_b128 v[180:183], v147 offset:49152
	ds_read_b128 v[184:187], v147 offset:50176
	ds_read_b128 v[188:191], v147 offset:51200
	ds_read_b128 v[192:195], v147 offset:52224
	ds_read_b128 v[196:199], v147 offset:53248
	ds_read_b128 v[200:203], v147 offset:54272
	ds_read_b128 v[204:207], v147 offset:55296
	ds_read_b128 v[208:211], v147 offset:56320
	global_load_lds_dwordx4 v[142:143], off
	s_add_i32 m0, s72, 0x2000
	s_add_u32 s70, s70, 0x40080
	v_lshl_add_u64 v[142:143], v[212:213], 0, s[12:13]
	s_addc_u32 s71, s71, 0
	s_add_i32 s72, s75, s49
	global_load_lds_dwordx4 v[142:143], off
	v_lshl_add_u64 v[142:143], s[70:71], 0, v[130:131]
	s_mov_b32 m0, s72
	s_nop 0
	global_load_lds_dwordx4 v[142:143], off
	v_lshl_add_u64 v[142:143], s[70:71], 0, v[132:133]
	s_add_i32 m0, s72, 0x2000
	s_nop 0
	global_load_lds_dwordx4 v[142:143], off
	v_lshl_add_u64 v[142:143], v[214:215], 0, s[12:13]
	s_mov_b32 m0, s83
	s_nop 0
	global_load_lds_dwordx4 v[142:143], off
	v_lshl_add_u64 v[142:143], v[216:217], 0, s[12:13]
	s_mov_b32 m0, s84
	s_nop 0
	global_load_lds_dwordx4 v[142:143], off
	s_waitcnt vmcnt(8)
	s_waitcnt lgkmcnt(0)
	s_setprio 1
	s_barrier
	v_mfma_f32_16x16x32_bf16 v[62:65], v[148:151], v[180:183], v[62:65]
	v_mfma_f32_16x16x32_bf16 v[58:61], v[156:159], v[180:183], v[58:61]
	v_mfma_f32_16x16x32_bf16 v[46:49], v[148:151], v[188:191], v[46:49]
	v_mfma_f32_16x16x32_bf16 v[42:45], v[156:159], v[188:191], v[42:45]
	v_mfma_f32_16x16x32_bf16 v[30:33], v[148:151], v[196:199], v[30:33]
	v_mfma_f32_16x16x32_bf16 v[26:29], v[156:159], v[196:199], v[26:29]
	v_mfma_f32_16x16x32_bf16 v[14:17], v[148:151], v[204:207], v[14:17]
	v_mfma_f32_16x16x32_bf16 v[10:13], v[156:159], v[204:207], v[10:13]
	v_mfma_f32_16x16x32_bf16 v[62:65], v[152:155], v[184:187], v[62:65]
	v_mfma_f32_16x16x32_bf16 v[58:61], v[160:163], v[184:187], v[58:61]
	v_mfma_f32_16x16x32_bf16 v[46:49], v[152:155], v[192:195], v[46:49]
	v_mfma_f32_16x16x32_bf16 v[42:45], v[160:163], v[192:195], v[42:45]
	v_mfma_f32_16x16x32_bf16 v[30:33], v[152:155], v[200:203], v[30:33]
	v_mfma_f32_16x16x32_bf16 v[26:29], v[160:163], v[200:203], v[26:29]
	v_mfma_f32_16x16x32_bf16 v[14:17], v[152:155], v[208:211], v[14:17]
	v_mfma_f32_16x16x32_bf16 v[10:13], v[160:163], v[208:211], v[10:13]
	v_mfma_f32_16x16x32_bf16 v[54:57], v[164:167], v[180:183], v[54:57]
	v_mfma_f32_16x16x32_bf16 v[50:53], v[172:175], v[180:183], v[50:53]
	v_mfma_f32_16x16x32_bf16 v[38:41], v[164:167], v[188:191], v[38:41]
	v_mfma_f32_16x16x32_bf16 v[34:37], v[172:175], v[188:191], v[34:37]
	v_mfma_f32_16x16x32_bf16 v[22:25], v[164:167], v[196:199], v[22:25]
	v_mfma_f32_16x16x32_bf16 v[18:21], v[172:175], v[196:199], v[18:21]
	v_mfma_f32_16x16x32_bf16 v[6:9], v[164:167], v[204:207], v[6:9]
	v_mfma_f32_16x16x32_bf16 v[2:5], v[172:175], v[204:207], v[2:5]
	v_mfma_f32_16x16x32_bf16 v[54:57], v[168:171], v[184:187], v[54:57]
	v_mfma_f32_16x16x32_bf16 v[50:53], v[176:179], v[184:187], v[50:53]
	v_mfma_f32_16x16x32_bf16 v[38:41], v[168:171], v[192:195], v[38:41]
	v_mfma_f32_16x16x32_bf16 v[34:37], v[176:179], v[192:195], v[34:37]
	v_mfma_f32_16x16x32_bf16 v[22:25], v[168:171], v[200:203], v[22:25]
	v_mfma_f32_16x16x32_bf16 v[18:21], v[176:179], v[200:203], v[18:21]
	v_mfma_f32_16x16x32_bf16 v[6:9], v[168:171], v[208:211], v[6:9]
	v_mfma_f32_16x16x32_bf16 v[2:5], v[176:179], v[208:211], v[2:5]
	s_barrier
	s_setprio 0
	s_add_i32 s70, s95, 2
	s_cmp_gt_u32 s95, 13
	s_mov_b32 s95, s70
	s_cbranch_scc1 .LBB0_1903

.LBB0_2030:
	s_or_b32 s18, s85, 1
	v_add_u32_e32 v111, s78, v147
	s_lshl_b64 s[36:37], s[18:19], 7
	s_add_i32 s18, s85, 2
	ds_read_b128 v[150:153], v111
	ds_read_b128 v[154:157], v111 offset:1024
	ds_read_b128 v[158:161], v111 offset:2048
	ds_read_b128 v[162:165], v111 offset:3072
	v_add_u32_e32 v111, s79, v147
	s_lshl_b64 s[38:39], s[18:19], 7
	ds_read_b128 v[168:171], v111
	ds_read_b128 v[172:175], v111 offset:1024
	ds_read_b128 v[176:179], v111 offset:2048
	ds_read_b128 v[180:183], v111 offset:3072
	s_add_u32 s68, s14, s38
	s_addc_u32 s69, s15, s39
	s_and_b64 s[34:35], s[30:31], exec
	s_cselect_b32 s35, s23, s69
	s_cselect_b32 s34, s81, s68
	s_add_u32 s38, s12, s38
	s_addc_u32 s39, s13, s39
	s_and_b64 s[30:31], s[30:31], exec
	s_cselect_b32 s31, s21, s39
	s_cselect_b32 s30, s82, s38
	s_add_u32 s36, s83, s36
	s_addc_u32 s37, s84, s37
	v_lshl_add_u64 v[112:113], s[36:37], 0, v[138:139]
	s_add_i32 m0, s11, 0xc000
	ds_read_b128 v[184:187], v148
	ds_read_b128 v[188:191], v148 offset:1024
	ds_read_b128 v[192:195], v148 offset:2048
	ds_read_b128 v[196:199], v148 offset:3072
	ds_read_b128 v[200:203], v148 offset:4096
	ds_read_b128 v[204:207], v148 offset:5120
	ds_read_b128 v[208:211], v148 offset:6144
	ds_read_b128 v[212:215], v148 offset:7168
	global_load_lds_dwordx4 v[112:113], off
	v_lshl_add_u64 v[112:113], s[36:37], 0, v[140:141]
	s_add_i32 m0, s11, 0xe000
	s_nop 0
	global_load_lds_dwordx4 v[112:113], off
	s_waitcnt vmcnt(8)
	s_waitcnt lgkmcnt(0)
	s_setprio 1
	s_barrier
	v_mfma_f32_16x16x32_bf16 v[130:133], v[150:153], v[184:187], v[130:133]
	v_mfma_f32_16x16x32_bf16 v[126:129], v[158:161], v[184:187], v[126:129]
	v_mfma_f32_16x16x32_bf16 v[112:115], v[150:153], v[192:195], v[114:117]
	v_mfma_f32_16x16x32_bf16 v[106:109], v[158:161], v[192:195], v[106:109]
	v_mfma_f32_16x16x32_bf16 v[94:97], v[150:153], v[200:203], v[94:97]
	v_mfma_f32_16x16x32_bf16 v[90:93], v[158:161], v[200:203], v[90:93]
	v_mfma_f32_16x16x32_bf16 v[78:81], v[150:153], v[208:211], v[78:81]
	v_mfma_f32_16x16x32_bf16 v[74:77], v[158:161], v[208:211], v[74:77]
	v_mfma_f32_16x16x32_bf16 v[130:133], v[154:157], v[188:191], v[130:133]
	v_mfma_f32_16x16x32_bf16 v[126:129], v[162:165], v[188:191], v[126:129]
	v_mfma_f32_16x16x32_bf16 v[112:115], v[154:157], v[196:199], v[112:115]
	v_mfma_f32_16x16x32_bf16 v[106:109], v[162:165], v[196:199], v[106:109]
	v_mfma_f32_16x16x32_bf16 v[94:97], v[154:157], v[204:207], v[94:97]
	v_mfma_f32_16x16x32_bf16 v[90:93], v[162:165], v[204:207], v[90:93]
	v_mfma_f32_16x16x32_bf16 v[78:81], v[154:157], v[212:215], v[78:81]
	v_mfma_f32_16x16x32_bf16 v[74:77], v[162:165], v[212:215], v[74:77]
	v_mfma_f32_16x16x32_bf16 v[122:125], v[168:171], v[184:187], v[122:125]
	v_mfma_f32_16x16x32_bf16 v[116:119], v[176:179], v[184:187], v[118:121]
	v_mfma_f32_16x16x32_bf16 v[102:105], v[168:171], v[192:195], v[102:105]
	v_mfma_f32_16x16x32_bf16 v[98:101], v[176:179], v[192:195], v[98:101]
	v_mfma_f32_16x16x32_bf16 v[86:89], v[168:171], v[200:203], v[86:89]
	v_mfma_f32_16x16x32_bf16 v[82:85], v[176:179], v[200:203], v[82:85]
	v_mfma_f32_16x16x32_bf16 v[70:73], v[168:171], v[208:211], v[70:73]
	v_mfma_f32_16x16x32_bf16 v[66:69], v[176:179], v[208:211], v[66:69]
	v_mfma_f32_16x16x32_bf16 v[122:125], v[172:175], v[188:191], v[122:125]
	v_mfma_f32_16x16x32_bf16 v[118:121], v[180:183], v[188:191], v[116:119]
	v_mfma_f32_16x16x32_bf16 v[102:105], v[172:175], v[196:199], v[102:105]
	v_mfma_f32_16x16x32_bf16 v[98:101], v[180:183], v[196:199], v[98:101]
	v_mfma_f32_16x16x32_bf16 v[86:89], v[172:175], v[204:207], v[86:89]
	v_mfma_f32_16x16x32_bf16 v[82:85], v[180:183], v[204:207], v[82:85]
	v_mfma_f32_16x16x32_bf16 v[70:73], v[172:175], v[212:215], v[70:73]
	v_mfma_f32_16x16x32_bf16 v[66:69], v[180:183], v[212:215], v[66:69]
	s_barrier
	s_setprio 0
	s_add_i32 s36, s78, s71
	v_lshl_add_u64 v[216:217], s[30:31], 0, v[134:135]
	s_mov_b32 m0, s36
	ds_read_b128 v[184:187], v148 offset:16384
	ds_read_b128 v[188:191], v148 offset:17408
	ds_read_b128 v[192:195], v148 offset:18432
	ds_read_b128 v[196:199], v148 offset:19456
	ds_read_b128 v[200:203], v148 offset:20480
	ds_read_b128 v[204:207], v148 offset:21504
	ds_read_b128 v[208:211], v148 offset:22528
	ds_read_b128 v[212:215], v148 offset:23552
	global_load_lds_dwordx4 v[216:217], off
	s_add_i32 m0, s36, 0x2000
	s_add_u32 s36, s30, 0x100000
	v_lshl_add_u64 v[218:219], s[30:31], 0, v[136:137]
	s_addc_u32 s37, s31, 0
	s_add_i32 s38, s79, s71
	global_load_lds_dwordx4 v[218:219], off
	v_lshl_add_u64 v[116:117], s[36:37], 0, v[134:135]
	s_mov_b32 m0, s38
	v_lshl_add_u64 v[220:221], s[34:35], 0, v[138:139]
	global_load_lds_dwordx4 v[116:117], off
	v_lshl_add_u64 v[116:117], s[36:37], 0, v[136:137]
	s_add_i32 m0, s38, 0x2000
	v_lshl_add_u64 v[222:223], s[34:35], 0, v[140:141]
	global_load_lds_dwordx4 v[116:117], off
	s_mov_b32 m0, s11
	s_nop 0
	global_load_lds_dwordx4 v[220:221], off
	s_mov_b32 m0, s72
	s_nop 0
	global_load_lds_dwordx4 v[222:223], off
	s_waitcnt vmcnt(8)
	s_waitcnt lgkmcnt(0)
	s_setprio 1
	s_barrier
	v_mfma_f32_16x16x32_bf16 v[62:65], v[150:153], v[184:187], v[62:65]
	v_mfma_f32_16x16x32_bf16 v[58:61], v[158:161], v[184:187], v[58:61]
	v_mfma_f32_16x16x32_bf16 v[46:49], v[150:153], v[192:195], v[46:49]
	v_mfma_f32_16x16x32_bf16 v[42:45], v[158:161], v[192:195], v[42:45]
	v_mfma_f32_16x16x32_bf16 v[30:33], v[150:153], v[200:203], v[30:33]
	v_mfma_f32_16x16x32_bf16 v[26:29], v[158:161], v[200:203], v[26:29]
	v_mfma_f32_16x16x32_bf16 v[14:17], v[150:153], v[208:211], v[14:17]
	v_mfma_f32_16x16x32_bf16 v[10:13], v[158:161], v[208:211], v[10:13]
	v_mfma_f32_16x16x32_bf16 v[62:65], v[154:157], v[188:191], v[62:65]
	v_mfma_f32_16x16x32_bf16 v[58:61], v[162:165], v[188:191], v[58:61]
	v_mfma_f32_16x16x32_bf16 v[46:49], v[154:157], v[196:199], v[46:49]
	v_mfma_f32_16x16x32_bf16 v[42:45], v[162:165], v[196:199], v[42:45]
	v_mfma_f32_16x16x32_bf16 v[30:33], v[154:157], v[204:207], v[30:33]
	v_mfma_f32_16x16x32_bf16 v[26:29], v[162:165], v[204:207], v[26:29]
	v_mfma_f32_16x16x32_bf16 v[14:17], v[154:157], v[212:215], v[14:17]
	v_mfma_f32_16x16x32_bf16 v[10:13], v[162:165], v[212:215], v[10:13]
	v_mfma_f32_16x16x32_bf16 v[54:57], v[168:171], v[184:187], v[54:57]
	v_mfma_f32_16x16x32_bf16 v[50:53], v[176:179], v[184:187], v[50:53]
	v_mfma_f32_16x16x32_bf16 v[38:41], v[168:171], v[192:195], v[38:41]
	v_mfma_f32_16x16x32_bf16 v[34:37], v[176:179], v[192:195], v[34:37]
	v_mfma_f32_16x16x32_bf16 v[22:25], v[168:171], v[200:203], v[22:25]
	v_mfma_f32_16x16x32_bf16 v[18:21], v[176:179], v[200:203], v[18:21]
	v_mfma_f32_16x16x32_bf16 v[6:9], v[168:171], v[208:211], v[6:9]
	v_mfma_f32_16x16x32_bf16 v[2:5], v[176:179], v[208:211], v[2:5]
	v_mfma_f32_16x16x32_bf16 v[54:57], v[172:175], v[188:191], v[54:57]
	v_mfma_f32_16x16x32_bf16 v[50:53], v[180:183], v[188:191], v[50:53]
	v_mfma_f32_16x16x32_bf16 v[38:41], v[172:175], v[196:199], v[38:41]
	v_mfma_f32_16x16x32_bf16 v[34:37], v[180:183], v[196:199], v[34:37]
	v_mfma_f32_16x16x32_bf16 v[22:25], v[172:175], v[204:207], v[22:25]
	v_mfma_f32_16x16x32_bf16 v[18:21], v[180:183], v[204:207], v[18:21]
	v_mfma_f32_16x16x32_bf16 v[6:9], v[172:175], v[212:215], v[6:9]
	v_mfma_f32_16x16x32_bf16 v[2:5], v[180:183], v[212:215], v[2:5]
	s_barrier
	s_setprio 0
	s_add_i32 s36, 0, 0x18000
	v_add_u32_e32 v111, s36, v147
	s_add_i32 s37, 0, 0x1c000
	ds_read_b128 v[150:153], v111
	ds_read_b128 v[154:157], v111 offset:1024
	ds_read_b128 v[158:161], v111 offset:2048
	ds_read_b128 v[162:165], v111 offset:3072
	v_add_u32_e32 v111, s37, v147
	ds_read_b128 v[168:171], v111
	ds_read_b128 v[172:175], v111 offset:1024
	ds_read_b128 v[176:179], v111 offset:2048
	ds_read_b128 v[180:183], v111 offset:3072
	s_add_u32 s34, s34, 0x100000
	s_addc_u32 s35, s35, 0
	s_mov_b32 m0, s73
	v_lshl_add_u64 v[116:117], s[34:35], 0, v[138:139]
	ds_read_b128 v[184:187], v148 offset:32768
	ds_read_b128 v[188:191], v148 offset:33792
	ds_read_b128 v[192:195], v148 offset:34816
	ds_read_b128 v[196:199], v148 offset:35840
	ds_read_b128 v[200:203], v148 offset:36864
	ds_read_b128 v[204:207], v148 offset:37888
	ds_read_b128 v[208:211], v148 offset:38912
	ds_read_b128 v[212:215], v148 offset:39936
	global_load_lds_dwordx4 v[116:117], off
	v_lshl_add_u64 v[116:117], s[34:35], 0, v[140:141]
	s_mov_b32 m0, s75
	s_nop 0
	global_load_lds_dwordx4 v[116:117], off
	s_waitcnt vmcnt(8)
	s_waitcnt lgkmcnt(0)
	s_setprio 1
	s_barrier
	v_mfma_f32_16x16x32_bf16 v[130:133], v[150:153], v[184:187], v[130:133]
	v_mfma_f32_16x16x32_bf16 v[126:129], v[158:161], v[184:187], v[126:129]
	v_mfma_f32_16x16x32_bf16 v[112:115], v[150:153], v[192:195], v[112:115]
	v_mfma_f32_16x16x32_bf16 v[106:109], v[158:161], v[192:195], v[106:109]
	v_mfma_f32_16x16x32_bf16 v[94:97], v[150:153], v[200:203], v[94:97]
	v_mfma_f32_16x16x32_bf16 v[90:93], v[158:161], v[200:203], v[90:93]
	v_mfma_f32_16x16x32_bf16 v[78:81], v[150:153], v[208:211], v[78:81]
	v_mfma_f32_16x16x32_bf16 v[74:77], v[158:161], v[208:211], v[74:77]
	v_mfma_f32_16x16x32_bf16 v[130:133], v[154:157], v[188:191], v[130:133]
	v_mfma_f32_16x16x32_bf16 v[126:129], v[162:165], v[188:191], v[126:129]
	v_mfma_f32_16x16x32_bf16 v[114:117], v[154:157], v[196:199], v[112:115]
	v_mfma_f32_16x16x32_bf16 v[106:109], v[162:165], v[196:199], v[106:109]
	v_mfma_f32_16x16x32_bf16 v[94:97], v[154:157], v[204:207], v[94:97]
	v_mfma_f32_16x16x32_bf16 v[90:93], v[162:165], v[204:207], v[90:93]
	v_mfma_f32_16x16x32_bf16 v[78:81], v[154:157], v[212:215], v[78:81]
	v_mfma_f32_16x16x32_bf16 v[74:77], v[162:165], v[212:215], v[74:77]
	v_mfma_f32_16x16x32_bf16 v[122:125], v[168:171], v[184:187], v[122:125]
	v_mfma_f32_16x16x32_bf16 v[118:121], v[176:179], v[184:187], v[118:121]
	v_mfma_f32_16x16x32_bf16 v[102:105], v[168:171], v[192:195], v[102:105]
	v_mfma_f32_16x16x32_bf16 v[98:101], v[176:179], v[192:195], v[98:101]
	v_mfma_f32_16x16x32_bf16 v[86:89], v[168:171], v[200:203], v[86:89]
	v_mfma_f32_16x16x32_bf16 v[82:85], v[176:179], v[200:203], v[82:85]
	v_mfma_f32_16x16x32_bf16 v[70:73], v[168:171], v[208:211], v[70:73]
	v_mfma_f32_16x16x32_bf16 v[66:69], v[176:179], v[208:211], v[66:69]
	v_mfma_f32_16x16x32_bf16 v[122:125], v[172:175], v[188:191], v[122:125]
	v_mfma_f32_16x16x32_bf16 v[118:121], v[180:183], v[188:191], v[118:121]
	v_mfma_f32_16x16x32_bf16 v[102:105], v[172:175], v[196:199], v[102:105]
	v_mfma_f32_16x16x32_bf16 v[98:101], v[180:183], v[196:199], v[98:101]
	v_mfma_f32_16x16x32_bf16 v[86:89], v[172:175], v[204:207], v[86:89]
	v_mfma_f32_16x16x32_bf16 v[82:85], v[180:183], v[204:207], v[82:85]
	v_mfma_f32_16x16x32_bf16 v[70:73], v[172:175], v[212:215], v[70:73]
	v_mfma_f32_16x16x32_bf16 v[66:69], v[180:183], v[212:215], v[66:69]
	s_barrier
	s_setprio 0
	s_add_i32 s34, s36, s71
	v_lshl_add_u64 v[112:113], v[216:217], 0, s[16:17]
	s_mov_b32 m0, s34
	ds_read_b128 v[184:187], v148 offset:49152
	ds_read_b128 v[188:191], v148 offset:50176
	ds_read_b128 v[192:195], v148 offset:51200
	ds_read_b128 v[196:199], v148 offset:52224
	ds_read_b128 v[200:203], v148 offset:53248
	ds_read_b128 v[204:207], v148 offset:54272
	ds_read_b128 v[208:211], v148 offset:55296
	ds_read_b128 v[212:215], v148 offset:56320
	global_load_lds_dwordx4 v[112:113], off
	s_add_i32 m0, s34, 0x2000
	s_add_u32 s30, s30, 0x100080
	v_lshl_add_u64 v[112:113], v[218:219], 0, s[16:17]
	s_addc_u32 s31, s31, 0
	s_add_i32 s34, s37, s71
	global_load_lds_dwordx4 v[112:113], off
	v_lshl_add_u64 v[112:113], s[30:31], 0, v[134:135]
	s_mov_b32 m0, s34
	s_nop 0
	global_load_lds_dwordx4 v[112:113], off
	v_lshl_add_u64 v[112:113], s[30:31], 0, v[136:137]
	s_add_i32 m0, s34, 0x2000
	s_nop 0
	global_load_lds_dwordx4 v[112:113], off
	v_lshl_add_u64 v[112:113], v[220:221], 0, s[16:17]
	s_mov_b32 m0, s76
	s_nop 0
	global_load_lds_dwordx4 v[112:113], off
	v_lshl_add_u64 v[112:113], v[222:223], 0, s[16:17]
	s_mov_b32 m0, s77
	s_nop 0
	global_load_lds_dwordx4 v[112:113], off
	s_waitcnt vmcnt(8)
	s_waitcnt lgkmcnt(0)
	s_setprio 1
	s_barrier
	v_mfma_f32_16x16x32_bf16 v[62:65], v[150:153], v[184:187], v[62:65]
	v_mfma_f32_16x16x32_bf16 v[58:61], v[158:161], v[184:187], v[58:61]
	v_mfma_f32_16x16x32_bf16 v[46:49], v[150:153], v[192:195], v[46:49]
	v_mfma_f32_16x16x32_bf16 v[42:45], v[158:161], v[192:195], v[42:45]
	v_mfma_f32_16x16x32_bf16 v[30:33], v[150:153], v[200:203], v[30:33]
	v_mfma_f32_16x16x32_bf16 v[26:29], v[158:161], v[200:203], v[26:29]
	v_mfma_f32_16x16x32_bf16 v[14:17], v[150:153], v[208:211], v[14:17]
	v_mfma_f32_16x16x32_bf16 v[10:13], v[158:161], v[208:211], v[10:13]
	v_mfma_f32_16x16x32_bf16 v[62:65], v[154:157], v[188:191], v[62:65]
	v_mfma_f32_16x16x32_bf16 v[58:61], v[162:165], v[188:191], v[58:61]
	v_mfma_f32_16x16x32_bf16 v[46:49], v[154:157], v[196:199], v[46:49]
	v_mfma_f32_16x16x32_bf16 v[42:45], v[162:165], v[196:199], v[42:45]
	v_mfma_f32_16x16x32_bf16 v[30:33], v[154:157], v[204:207], v[30:33]
	v_mfma_f32_16x16x32_bf16 v[26:29], v[162:165], v[204:207], v[26:29]
	v_mfma_f32_16x16x32_bf16 v[14:17], v[154:157], v[212:215], v[14:17]
	v_mfma_f32_16x16x32_bf16 v[10:13], v[162:165], v[212:215], v[10:13]
	v_mfma_f32_16x16x32_bf16 v[54:57], v[168:171], v[184:187], v[54:57]
	v_mfma_f32_16x16x32_bf16 v[50:53], v[176:179], v[184:187], v[50:53]
	v_mfma_f32_16x16x32_bf16 v[38:41], v[168:171], v[192:195], v[38:41]
	v_mfma_f32_16x16x32_bf16 v[34:37], v[176:179], v[192:195], v[34:37]
	v_mfma_f32_16x16x32_bf16 v[22:25], v[168:171], v[200:203], v[22:25]
	v_mfma_f32_16x16x32_bf16 v[18:21], v[176:179], v[200:203], v[18:21]
	v_mfma_f32_16x16x32_bf16 v[6:9], v[168:171], v[208:211], v[6:9]
	v_mfma_f32_16x16x32_bf16 v[2:5], v[176:179], v[208:211], v[2:5]
	v_mfma_f32_16x16x32_bf16 v[54:57], v[172:175], v[188:191], v[54:57]
	v_mfma_f32_16x16x32_bf16 v[50:53], v[180:183], v[188:191], v[50:53]
	v_mfma_f32_16x16x32_bf16 v[38:41], v[172:175], v[196:199], v[38:41]
	v_mfma_f32_16x16x32_bf16 v[34:37], v[180:183], v[196:199], v[34:37]
	v_mfma_f32_16x16x32_bf16 v[22:25], v[172:175], v[204:207], v[22:25]
	v_mfma_f32_16x16x32_bf16 v[18:21], v[180:183], v[204:207], v[18:21]
	v_mfma_f32_16x16x32_bf16 v[6:9], v[172:175], v[212:215], v[6:9]
	v_mfma_f32_16x16x32_bf16 v[2:5], v[180:183], v[212:215], v[2:5]
	s_barrier
	s_setprio 0
	s_cmp_gt_u32 s85, 61
	s_cbranch_scc1 .LBB0_2032
	s_mov_b32 s85, s18
	s_branch .LBB0_2015

.LBB0_2156:
	s_lshl_b32 s38, s73, 7
	s_add_u32 s39, s28, s38
	s_addc_u32 s42, s29, 0
	s_add_u32 s43, s39, 0x100
	v_add_u32_e32 v76, s69, v188
	v_add_u32_e32 v156, s70, v188
	s_addc_u32 s46, s42, 0
	ds_read_b128 v[64:67], v76
	ds_read_b128 v[68:71], v76 offset:1024
	ds_read_b128 v[72:75], v76 offset:2048
	ds_read_b128 v[76:79], v76 offset:3072
	ds_read_b128 v[144:147], v156
	ds_read_b128 v[148:151], v156 offset:1024
	ds_read_b128 v[152:155], v156 offset:2048
	ds_read_b128 v[156:159], v156 offset:3072
	s_and_b64 s[36:37], s[34:35], exec
	s_cselect_b32 s37, s17, s46
	s_cselect_b32 s36, s71, s43
	s_add_u32 s38, s26, s38
	s_addc_u32 s43, s27, 0
	s_add_u32 s38, s38, 0x100
	s_addc_u32 s43, s43, 0
	s_and_b64 s[34:35], s[34:35], exec
	s_cselect_b32 s35, s15, s43
	s_cselect_b32 s34, s72, s38
	s_add_u32 s38, s39, 0x40080
	s_addc_u32 s39, s42, 0
	v_lshl_add_u64 v[186:187], s[38:39], 0, v[172:173]
	s_add_i32 m0, s23, 0xc000
	ds_read_b128 v[160:163], v191
	ds_read_b128 v[164:167], v191 offset:1024
	ds_read_b128 v[180:183], v191 offset:2048
	ds_read_b128 v[194:197], v191 offset:3072
	ds_read_b128 v[198:201], v191 offset:4096
	ds_read_b128 v[202:205], v191 offset:5120
	ds_read_b128 v[206:209], v191 offset:6144
	ds_read_b128 v[210:213], v191 offset:7168
	global_load_lds_dwordx4 v[186:187], off
	v_lshl_add_u64 v[186:187], s[38:39], 0, v[174:175]
	s_add_i32 m0, s23, 0xe000
	s_nop 0
	global_load_lds_dwordx4 v[186:187], off
	s_waitcnt vmcnt(8)
	s_waitcnt lgkmcnt(0)
	s_setprio 1
	s_barrier
	v_mfma_f32_16x16x32_bf16 v[140:143], v[64:67], v[160:163], v[140:143]
	v_mfma_f32_16x16x32_bf16 v[136:139], v[72:75], v[160:163], v[136:139]
	v_mfma_f32_16x16x32_bf16 v[124:127], v[64:67], v[180:183], v[124:127]
	v_mfma_f32_16x16x32_bf16 v[120:123], v[72:75], v[180:183], v[120:123]
	v_mfma_f32_16x16x32_bf16 v[108:111], v[64:67], v[198:201], v[108:111]
	v_mfma_f32_16x16x32_bf16 v[104:107], v[72:75], v[198:201], v[104:107]
	v_mfma_f32_16x16x32_bf16 v[92:95], v[64:67], v[206:209], v[92:95]
	v_mfma_f32_16x16x32_bf16 v[88:91], v[72:75], v[206:209], v[88:91]
	v_mfma_f32_16x16x32_bf16 v[140:143], v[68:71], v[164:167], v[140:143]
	v_mfma_f32_16x16x32_bf16 v[136:139], v[76:79], v[164:167], v[136:139]
	v_mfma_f32_16x16x32_bf16 v[124:127], v[68:71], v[194:197], v[124:127]
	v_mfma_f32_16x16x32_bf16 v[120:123], v[76:79], v[194:197], v[120:123]
	v_mfma_f32_16x16x32_bf16 v[108:111], v[68:71], v[202:205], v[108:111]
	v_mfma_f32_16x16x32_bf16 v[104:107], v[76:79], v[202:205], v[104:107]
	v_mfma_f32_16x16x32_bf16 v[92:95], v[68:71], v[210:213], v[92:95]
	v_mfma_f32_16x16x32_bf16 v[88:91], v[76:79], v[210:213], v[88:91]
	v_mfma_f32_16x16x32_bf16 v[132:135], v[144:147], v[160:163], v[132:135]
	v_mfma_f32_16x16x32_bf16 v[128:131], v[152:155], v[160:163], v[128:131]
	v_mfma_f32_16x16x32_bf16 v[116:119], v[144:147], v[180:183], v[116:119]
	v_mfma_f32_16x16x32_bf16 v[112:115], v[152:155], v[180:183], v[112:115]
	v_mfma_f32_16x16x32_bf16 v[100:103], v[144:147], v[198:201], v[100:103]
	v_mfma_f32_16x16x32_bf16 v[96:99], v[152:155], v[198:201], v[96:99]
	v_mfma_f32_16x16x32_bf16 v[84:87], v[144:147], v[206:209], v[84:87]
	v_mfma_f32_16x16x32_bf16 v[80:83], v[152:155], v[206:209], v[80:83]
	v_mfma_f32_16x16x32_bf16 v[132:135], v[148:151], v[164:167], v[132:135]
	v_mfma_f32_16x16x32_bf16 v[128:131], v[156:159], v[164:167], v[128:131]
	v_mfma_f32_16x16x32_bf16 v[116:119], v[148:151], v[194:197], v[116:119]
	v_mfma_f32_16x16x32_bf16 v[112:115], v[156:159], v[194:197], v[112:115]
	v_mfma_f32_16x16x32_bf16 v[100:103], v[148:151], v[202:205], v[100:103]
	v_mfma_f32_16x16x32_bf16 v[96:99], v[156:159], v[202:205], v[96:99]
	v_mfma_f32_16x16x32_bf16 v[84:87], v[148:151], v[210:213], v[84:87]
	v_mfma_f32_16x16x32_bf16 v[80:83], v[156:159], v[210:213], v[80:83]
	s_barrier
	s_setprio 0
	s_add_i32 s38, s69, s54
	v_lshl_add_u64 v[186:187], s[34:35], 0, v[168:169]
	s_mov_b32 m0, s38
	ds_read_b128 v[160:163], v191 offset:16384
	ds_read_b128 v[164:167], v191 offset:17408
	ds_read_b128 v[180:183], v191 offset:18432
	ds_read_b128 v[194:197], v191 offset:19456
	ds_read_b128 v[198:201], v191 offset:20480
	ds_read_b128 v[202:205], v191 offset:21504
	ds_read_b128 v[206:209], v191 offset:22528
	ds_read_b128 v[210:213], v191 offset:23552
	global_load_lds_dwordx4 v[186:187], off
	s_add_i32 m0, s38, 0x2000
	s_add_u32 s38, s34, 0x40000
	v_lshl_add_u64 v[214:215], s[34:35], 0, v[170:171]
	s_addc_u32 s39, s35, 0
	s_add_i32 s42, s70, s54
	global_load_lds_dwordx4 v[214:215], off
	v_lshl_add_u64 v[216:217], s[38:39], 0, v[168:169]
	s_mov_b32 m0, s42
	v_lshl_add_u64 v[218:219], s[36:37], 0, v[174:175]
	global_load_lds_dwordx4 v[216:217], off
	v_lshl_add_u64 v[216:217], s[38:39], 0, v[170:171]
	s_add_i32 m0, s42, 0x2000
	s_nop 0
	global_load_lds_dwordx4 v[216:217], off
	v_lshl_add_u64 v[216:217], s[36:37], 0, v[172:173]
	s_mov_b32 m0, s23
	s_nop 0
	global_load_lds_dwordx4 v[216:217], off
	s_mov_b32 m0, s25
	s_nop 0
	global_load_lds_dwordx4 v[218:219], off
	s_waitcnt vmcnt(8)
	s_waitcnt lgkmcnt(0)
	s_setprio 1
	s_barrier
	v_mfma_f32_16x16x32_bf16 v[60:63], v[64:67], v[160:163], v[60:63]
	v_mfma_f32_16x16x32_bf16 v[56:59], v[72:75], v[160:163], v[56:59]
	v_mfma_f32_16x16x32_bf16 v[44:47], v[64:67], v[180:183], v[44:47]
	v_mfma_f32_16x16x32_bf16 v[40:43], v[72:75], v[180:183], v[40:43]
	v_mfma_f32_16x16x32_bf16 v[28:31], v[64:67], v[198:201], v[28:31]
	v_mfma_f32_16x16x32_bf16 v[24:27], v[72:75], v[198:201], v[24:27]
	v_mfma_f32_16x16x32_bf16 v[12:15], v[64:67], v[206:209], v[12:15]
	v_mfma_f32_16x16x32_bf16 v[8:11], v[72:75], v[206:209], v[8:11]
	v_mfma_f32_16x16x32_bf16 v[60:63], v[68:71], v[164:167], v[60:63]
	v_mfma_f32_16x16x32_bf16 v[56:59], v[76:79], v[164:167], v[56:59]
	v_mfma_f32_16x16x32_bf16 v[44:47], v[68:71], v[194:197], v[44:47]
	v_mfma_f32_16x16x32_bf16 v[40:43], v[76:79], v[194:197], v[40:43]
	v_mfma_f32_16x16x32_bf16 v[28:31], v[68:71], v[202:205], v[28:31]
	v_mfma_f32_16x16x32_bf16 v[24:27], v[76:79], v[202:205], v[24:27]
	v_mfma_f32_16x16x32_bf16 v[12:15], v[68:71], v[210:213], v[12:15]
	v_mfma_f32_16x16x32_bf16 v[8:11], v[76:79], v[210:213], v[8:11]
	v_mfma_f32_16x16x32_bf16 v[52:55], v[144:147], v[160:163], v[52:55]
	v_mfma_f32_16x16x32_bf16 v[48:51], v[152:155], v[160:163], v[48:51]
	v_mfma_f32_16x16x32_bf16 v[36:39], v[144:147], v[180:183], v[36:39]
	v_mfma_f32_16x16x32_bf16 v[32:35], v[152:155], v[180:183], v[32:35]
	v_mfma_f32_16x16x32_bf16 v[20:23], v[144:147], v[198:201], v[20:23]
	v_mfma_f32_16x16x32_bf16 v[16:19], v[152:155], v[198:201], v[16:19]
	v_mfma_f32_16x16x32_bf16 v[4:7], v[144:147], v[206:209], v[4:7]
	v_mfma_f32_16x16x32_bf16 v[0:3], v[152:155], v[206:209], v[0:3]
	v_mfma_f32_16x16x32_bf16 v[52:55], v[148:151], v[164:167], v[52:55]
	v_mfma_f32_16x16x32_bf16 v[48:51], v[156:159], v[164:167], v[48:51]
	v_mfma_f32_16x16x32_bf16 v[36:39], v[148:151], v[194:197], v[36:39]
	v_mfma_f32_16x16x32_bf16 v[32:35], v[156:159], v[194:197], v[32:35]
	v_mfma_f32_16x16x32_bf16 v[20:23], v[148:151], v[202:205], v[20:23]
	v_mfma_f32_16x16x32_bf16 v[16:19], v[156:159], v[202:205], v[16:19]
	v_mfma_f32_16x16x32_bf16 v[4:7], v[148:151], v[210:213], v[4:7]
	v_mfma_f32_16x16x32_bf16 v[0:3], v[156:159], v[210:213], v[0:3]
	s_barrier
	s_setprio 0
	s_add_i32 s38, 0, 0x18000
	s_add_i32 s39, 0, 0x1c000
	v_add_u32_e32 v76, s38, v188
	v_add_u32_e32 v156, s39, v188
	ds_read_b128 v[64:67], v76
	ds_read_b128 v[68:71], v76 offset:1024
	ds_read_b128 v[72:75], v76 offset:2048
	ds_read_b128 v[76:79], v76 offset:3072
	ds_read_b128 v[144:147], v156
	ds_read_b128 v[148:151], v156 offset:1024
	ds_read_b128 v[152:155], v156 offset:2048
	ds_read_b128 v[156:159], v156 offset:3072
	s_add_u32 s36, s36, 0x40000
	s_addc_u32 s37, s37, 0
	s_mov_b32 m0, s55
	v_lshl_add_u64 v[220:221], s[36:37], 0, v[172:173]
	ds_read_b128 v[160:163], v191 offset:32768
	ds_read_b128 v[164:167], v191 offset:33792
	ds_read_b128 v[180:183], v191 offset:34816
	ds_read_b128 v[194:197], v191 offset:35840
	ds_read_b128 v[198:201], v191 offset:36864
	ds_read_b128 v[202:205], v191 offset:37888
	ds_read_b128 v[206:209], v191 offset:38912
	ds_read_b128 v[210:213], v191 offset:39936
	global_load_lds_dwordx4 v[220:221], off
	v_lshl_add_u64 v[220:221], s[36:37], 0, v[174:175]
	s_mov_b32 m0, s56
	s_nop 0
	global_load_lds_dwordx4 v[220:221], off
	s_waitcnt vmcnt(8)
	s_waitcnt lgkmcnt(0)
	s_setprio 1
	s_barrier
	v_mfma_f32_16x16x32_bf16 v[140:143], v[64:67], v[160:163], v[140:143]
	v_mfma_f32_16x16x32_bf16 v[136:139], v[72:75], v[160:163], v[136:139]
	v_mfma_f32_16x16x32_bf16 v[124:127], v[64:67], v[180:183], v[124:127]
	v_mfma_f32_16x16x32_bf16 v[120:123], v[72:75], v[180:183], v[120:123]
	v_mfma_f32_16x16x32_bf16 v[108:111], v[64:67], v[198:201], v[108:111]
	v_mfma_f32_16x16x32_bf16 v[104:107], v[72:75], v[198:201], v[104:107]
	v_mfma_f32_16x16x32_bf16 v[92:95], v[64:67], v[206:209], v[92:95]
	v_mfma_f32_16x16x32_bf16 v[88:91], v[72:75], v[206:209], v[88:91]
	v_mfma_f32_16x16x32_bf16 v[140:143], v[68:71], v[164:167], v[140:143]
	v_mfma_f32_16x16x32_bf16 v[136:139], v[76:79], v[164:167], v[136:139]
	v_mfma_f32_16x16x32_bf16 v[124:127], v[68:71], v[194:197], v[124:127]
	v_mfma_f32_16x16x32_bf16 v[120:123], v[76:79], v[194:197], v[120:123]
	v_mfma_f32_16x16x32_bf16 v[108:111], v[68:71], v[202:205], v[108:111]
	v_mfma_f32_16x16x32_bf16 v[104:107], v[76:79], v[202:205], v[104:107]
	v_mfma_f32_16x16x32_bf16 v[92:95], v[68:71], v[210:213], v[92:95]
	v_mfma_f32_16x16x32_bf16 v[88:91], v[76:79], v[210:213], v[88:91]
	v_mfma_f32_16x16x32_bf16 v[132:135], v[144:147], v[160:163], v[132:135]
	v_mfma_f32_16x16x32_bf16 v[128:131], v[152:155], v[160:163], v[128:131]
	v_mfma_f32_16x16x32_bf16 v[116:119], v[144:147], v[180:183], v[116:119]
	v_mfma_f32_16x16x32_bf16 v[112:115], v[152:155], v[180:183], v[112:115]
	v_mfma_f32_16x16x32_bf16 v[100:103], v[144:147], v[198:201], v[100:103]
	v_mfma_f32_16x16x32_bf16 v[96:99], v[152:155], v[198:201], v[96:99]
	v_mfma_f32_16x16x32_bf16 v[84:87], v[144:147], v[206:209], v[84:87]
	v_mfma_f32_16x16x32_bf16 v[80:83], v[152:155], v[206:209], v[80:83]
	v_mfma_f32_16x16x32_bf16 v[132:135], v[148:151], v[164:167], v[132:135]
	v_mfma_f32_16x16x32_bf16 v[128:131], v[156:159], v[164:167], v[128:131]
	v_mfma_f32_16x16x32_bf16 v[116:119], v[148:151], v[194:197], v[116:119]
	v_mfma_f32_16x16x32_bf16 v[112:115], v[156:159], v[194:197], v[112:115]
	v_mfma_f32_16x16x32_bf16 v[100:103], v[148:151], v[202:205], v[100:103]
	v_mfma_f32_16x16x32_bf16 v[96:99], v[156:159], v[202:205], v[96:99]
	v_mfma_f32_16x16x32_bf16 v[84:87], v[148:151], v[210:213], v[84:87]
	v_mfma_f32_16x16x32_bf16 v[80:83], v[156:159], v[210:213], v[80:83]
	s_barrier
	s_setprio 0
	s_add_i32 s36, s38, s54
	v_lshl_add_u64 v[186:187], v[186:187], 0, s[12:13]
	s_mov_b32 m0, s36
	ds_read_b128 v[160:163], v191 offset:49152
	ds_read_b128 v[164:167], v191 offset:50176
	ds_read_b128 v[180:183], v191 offset:51200
	ds_read_b128 v[194:197], v191 offset:52224
	ds_read_b128 v[198:201], v191 offset:53248
	ds_read_b128 v[202:205], v191 offset:54272
	ds_read_b128 v[206:209], v191 offset:55296
	ds_read_b128 v[210:213], v191 offset:56320
	global_load_lds_dwordx4 v[186:187], off
	s_add_i32 m0, s36, 0x2000
	s_add_u32 s34, s34, 0x40080
	v_lshl_add_u64 v[186:187], v[214:215], 0, s[12:13]
	s_addc_u32 s35, s35, 0
	s_add_i32 s36, s39, s54
	global_load_lds_dwordx4 v[186:187], off
	v_lshl_add_u64 v[186:187], s[34:35], 0, v[168:169]
	s_mov_b32 m0, s36
	s_nop 0
	global_load_lds_dwordx4 v[186:187], off
	v_lshl_add_u64 v[186:187], s[34:35], 0, v[170:171]
	s_add_i32 m0, s36, 0x2000
	s_nop 0
	global_load_lds_dwordx4 v[186:187], off
	v_lshl_add_u64 v[186:187], v[216:217], 0, s[12:13]
	s_mov_b32 m0, s57
	s_nop 0
	global_load_lds_dwordx4 v[186:187], off
	v_lshl_add_u64 v[186:187], v[218:219], 0, s[12:13]
	s_mov_b32 m0, s66
	s_nop 0
	global_load_lds_dwordx4 v[186:187], off
	s_waitcnt vmcnt(8)
	s_waitcnt lgkmcnt(0)
	s_setprio 1
	s_barrier
	v_mfma_f32_16x16x32_bf16 v[60:63], v[64:67], v[160:163], v[60:63]
	v_mfma_f32_16x16x32_bf16 v[56:59], v[72:75], v[160:163], v[56:59]
	v_mfma_f32_16x16x32_bf16 v[44:47], v[64:67], v[180:183], v[44:47]
	v_mfma_f32_16x16x32_bf16 v[40:43], v[72:75], v[180:183], v[40:43]
	v_mfma_f32_16x16x32_bf16 v[28:31], v[64:67], v[198:201], v[28:31]
	v_mfma_f32_16x16x32_bf16 v[24:27], v[72:75], v[198:201], v[24:27]
	v_mfma_f32_16x16x32_bf16 v[12:15], v[64:67], v[206:209], v[12:15]
	v_mfma_f32_16x16x32_bf16 v[8:11], v[72:75], v[206:209], v[8:11]
	v_mfma_f32_16x16x32_bf16 v[60:63], v[68:71], v[164:167], v[60:63]
	v_mfma_f32_16x16x32_bf16 v[56:59], v[76:79], v[164:167], v[56:59]
	v_mfma_f32_16x16x32_bf16 v[44:47], v[68:71], v[194:197], v[44:47]
	v_mfma_f32_16x16x32_bf16 v[40:43], v[76:79], v[194:197], v[40:43]
	v_mfma_f32_16x16x32_bf16 v[28:31], v[68:71], v[202:205], v[28:31]
	v_mfma_f32_16x16x32_bf16 v[24:27], v[76:79], v[202:205], v[24:27]
	v_mfma_f32_16x16x32_bf16 v[12:15], v[68:71], v[210:213], v[12:15]
	v_mfma_f32_16x16x32_bf16 v[8:11], v[76:79], v[210:213], v[8:11]
	v_mfma_f32_16x16x32_bf16 v[52:55], v[144:147], v[160:163], v[52:55]
	v_mfma_f32_16x16x32_bf16 v[48:51], v[152:155], v[160:163], v[48:51]
	v_mfma_f32_16x16x32_bf16 v[36:39], v[144:147], v[180:183], v[36:39]
	v_mfma_f32_16x16x32_bf16 v[32:35], v[152:155], v[180:183], v[32:35]
	v_mfma_f32_16x16x32_bf16 v[20:23], v[144:147], v[198:201], v[20:23]
	v_mfma_f32_16x16x32_bf16 v[16:19], v[152:155], v[198:201], v[16:19]
	v_mfma_f32_16x16x32_bf16 v[4:7], v[144:147], v[206:209], v[4:7]
	v_mfma_f32_16x16x32_bf16 v[0:3], v[152:155], v[206:209], v[0:3]
	v_mfma_f32_16x16x32_bf16 v[52:55], v[148:151], v[164:167], v[52:55]
	v_mfma_f32_16x16x32_bf16 v[48:51], v[156:159], v[164:167], v[48:51]
	v_mfma_f32_16x16x32_bf16 v[36:39], v[148:151], v[194:197], v[36:39]
	v_mfma_f32_16x16x32_bf16 v[32:35], v[156:159], v[194:197], v[32:35]
	v_mfma_f32_16x16x32_bf16 v[20:23], v[148:151], v[202:205], v[20:23]
	v_mfma_f32_16x16x32_bf16 v[16:19], v[156:159], v[202:205], v[16:19]
	v_mfma_f32_16x16x32_bf16 v[4:7], v[148:151], v[210:213], v[4:7]
	v_mfma_f32_16x16x32_bf16 v[0:3], v[156:159], v[210:213], v[0:3]
	s_barrier
	s_setprio 0
	s_add_i32 s34, s73, 2
	s_cmp_gt_u32 s73, 13
	s_mov_b32 s73, s34
	s_cbranch_scc1 .LBB0_2145
